# i4 + one static priority raise: per-segment s_setprio toggles removed from the GEMM K-loops, the wave half that takes the extra prologue barrier runs at priority 1 for the whole phase (reset at the gr
# baseline (speedup 1.0000x reference)
.LBB0_185:
	s_andn2_b64 vcc, exec, s[6:7]
	s_cbranch_vccnz .LBB0_221
	v_bfe_i32 v5, v1, 27, 1
	v_lshlrev_b32_e32 v4, 4, v1
	v_lshrrev_b32_e32 v5, 22, v5
	v_add_u32_e32 v5, v4, v5
	v_and_b32_e32 v5, 0xfffffc00, v5
	v_sub_u32_e32 v5, v4, v5
	v_lshrrev_b32_e32 v6, 4, v5
	v_ashrrev_i32_e32 v2, 31, v1
	v_bitop3_b32 v5, v6, v5, 32 bitop3:0x6c
	v_lshrrev_b32_e32 v2, 26, v2
	v_ashrrev_i32_e32 v7, 31, v5
	v_add_u32_e32 v2, v1, v2
	v_lshrrev_b32_e32 v7, 26, v7
	v_ashrrev_i32_e32 v2, 6, v2
	v_add_u32_e32 v7, v5, v7
	v_lshlrev_b32_e32 v6, 3, v2
	v_ashrrev_i32_e32 v12, 6, v7
	v_and_b32_e32 v7, 0xc0, v7
	v_and_b32_e32 v6, -16, v6
	v_sub_u32_e32 v5, v5, v7
	v_add_u32_e32 v6, v12, v6
	v_ashrrev_i16_sdwa v5, v216, sext(v5) dst_sel:DWORD dst_unused:UNUSED_PAD src0_sel:DWORD src1_sel:BYTE_0
	v_lshlrev_b32_e32 v8, 5, v2
	v_bfe_i32 v13, v5, 0, 16
	v_lshlrev_b32_e32 v5, 1, v6
	v_lshrrev_b32_e32 v7, 2, v6
	v_and_b32_e32 v9, 3, v12
	s_mov_b32 s0, 0xfffe0
	v_and_b32_e32 v8, 32, v8
	v_and_b32_e32 v5, 24, v5
	v_and_b32_e32 v7, 4, v7
	v_and_or_b32 v9, v6, s0, v9
	v_or3_b32 v5, v9, v7, v5
	v_add_lshl_u32 v7, v8, v13, 1
	v_add_u32_e32 v4, 0x2000, v4
	v_lshl_add_u32 v134, v5, 12, v7
	v_ashrrev_i32_e32 v5, 31, v4
	v_lshrrev_b32_e32 v5, 22, v5
	v_add_u32_e32 v5, v4, v5
	v_ashrrev_i32_e32 v14, 10, v5
	v_mul_i32_i24_e32 v5, 0x400, v14
	v_sub_u32_e32 v4, v4, v5
	v_lshrrev_b32_e32 v5, 4, v4
	v_bitop3_b32 v4, v5, v4, 32 bitop3:0x6c
	v_lshl_add_u32 v136, v6, 12, v7
	v_ashrrev_i32_e32 v6, 31, v4
	v_lshrrev_b32_e32 v6, 26, v6
	v_add_u32_e32 v6, v4, v6
	v_lshlrev_b32_e32 v5, 3, v14
	v_ashrrev_i32_e32 v15, 6, v6
	v_and_b32_e32 v6, 0xc0, v6
	s_ashr_i32 s10, s3, 6
	v_and_b32_e32 v5, -16, v5
	v_sub_u32_e32 v4, v4, v6
	v_add_u32_e32 v5, v15, v5
	v_ashrrev_i16_sdwa v4, v216, sext(v4) dst_sel:DWORD dst_unused:UNUSED_PAD src0_sel:DWORD src1_sel:BYTE_0
	s_lshl_b32 s31, s10, 10
	v_lshlrev_b32_e32 v7, 5, v14
	v_bfe_i32 v16, v4, 0, 16
	v_lshlrev_b32_e32 v4, 1, v5
	v_lshrrev_b32_e32 v6, 2, v5
	v_and_b32_e32 v8, 3, v15
	s_add_i32 s34, s31, 0
	v_and_b32_e32 v7, 32, v7
	v_and_b32_e32 v4, 24, v4
	v_and_b32_e32 v6, 4, v6
	v_and_or_b32 v8, v5, s0, v8
	s_waitcnt lgkmcnt(0)
	s_add_i32 m0, s34, 0x10000
	v_or3_b32 v4, v8, v6, v4
	v_add_lshl_u32 v6, v7, v16, 1
	s_ashr_i32 s11, s3, 8
	global_load_lds_dwordx4 v134, s[20:21]
	s_add_i32 m0, s34, 0x12000
	v_lshl_add_u32 v138, v4, 12, v6
	s_add_u32 s6, s20, 0x80000
	global_load_lds_dwordx4 v138, s[20:21]
	s_addc_u32 s7, s21, 0
	s_add_i32 m0, s34, 0x14000
	s_add_i32 s35, s34, 0x2000
	global_load_lds_dwordx4 v134, s[6:7]
	s_add_i32 m0, s34, 0x16000
	v_lshl_add_u32 v140, v5, 12, v6
	global_load_lds_dwordx4 v138, s[6:7]
	s_mov_b32 m0, s34
	s_add_u32 s6, s18, 0x80000
	global_load_lds_dwordx4 v136, s[18:19]
	s_mov_b32 m0, s35
	s_addc_u32 s7, s19, 0
	s_add_i32 s36, s34, 0x4000
	global_load_lds_dwordx4 v140, s[18:19]
	s_mov_b32 m0, s36
	s_add_i32 s37, s34, 0x6000
	global_load_lds_dwordx4 v136, s[6:7]
	s_mov_b32 m0, s37
	v_mov_b32_e32 v135, v3
	global_load_lds_dwordx4 v140, s[6:7]
	v_mov_b32_e32 v139, v3
	v_mov_b32_e32 v137, v3
	v_mov_b32_e32 v141, v3
	s_cmp_eq_u32 s11, 1
	v_lshl_add_u64 v[10:11], s[20:21], 0, v[134:135]
	v_lshl_add_u64 v[8:9], s[20:21], 0, v[138:139]
	v_lshl_add_u64 v[4:5], s[18:19], 0, v[136:137]
	s_cselect_b64 s[6:7], -1, 0
	s_cmp_lg_u32 s11, 1
	v_lshl_add_u64 v[6:7], s[18:19], 0, v[140:141]
	s_cbranch_scc1 .LBB0_188
	s_barrier
	s_setprio 1

.LBB0_198:
	s_add_u32 s20, s18, 0xfff80080
	s_addc_u32 s21, s19, -1
	s_add_i32 s49, 0, 0x10000
	s_cmp_eq_u32 s48, 28
	s_cselect_b32 s23, s15, s21
	s_cselect_b32 s22, s14, s20
	v_add_u32_e32 v2, s49, v1
	s_cselect_b32 s21, s17, s46
	s_cselect_b32 s20, s16, s3
	s_add_i32 s60, 0, 0x14000
	ds_read_b128 v[146:149], v2
	ds_read_b128 v[150:153], v2 offset:1024
	ds_read_b128 v[154:157], v2 offset:2048
	ds_read_b128 v[158:161], v2 offset:3072
	v_add_u32_e32 v2, s60, v1
	ds_read_b128 v[162:165], v2
	ds_read_b128 v[166:169], v2 offset:1024
	ds_read_b128 v[170:173], v2 offset:2048
	ds_read_b128 v[174:177], v2 offset:3072
	v_lshl_add_u64 v[194:195], s[18:19], 0, v[144:145]
	s_add_i32 m0, s34, 0xc000
	ds_read_b128 v[178:181], v133
	ds_read_b128 v[182:185], v133 offset:1024
	ds_read_b128 v[186:189], v133 offset:2048
	ds_read_b128 v[190:193], v133 offset:3072
	ds_read_b128 v[204:207], v133 offset:4096
	ds_read_b128 v[208:211], v133 offset:5120
	ds_read_b128 v[212:215], v133 offset:6144
	ds_read_b128 v[226:229], v133 offset:7168
	global_load_lds_dwordx4 v[194:195], off
	v_lshl_add_u64 v[194:195], s[18:19], 0, v[142:143]
	s_add_i32 m0, s34, 0xe000
	s_nop 0
	global_load_lds_dwordx4 v[194:195], off
	s_waitcnt vmcnt(8)
	s_waitcnt lgkmcnt(0)
	s_barrier
	s_nop 0
	s_waitcnt lgkmcnt(0)
	v_mfma_f32_16x16x32_bf16 v[128:131], v[146:149], v[178:181], v[128:131]
	v_mfma_f32_16x16x32_bf16 v[124:127], v[154:157], v[178:181], v[124:127]
	v_mfma_f32_16x16x32_bf16 v[112:115], v[146:149], v[186:189], v[112:115]
	v_mfma_f32_16x16x32_bf16 v[108:111], v[154:157], v[186:189], v[108:111]
	v_mfma_f32_16x16x32_bf16 v[96:99], v[146:149], v[204:207], v[96:99]
	v_mfma_f32_16x16x32_bf16 v[92:95], v[154:157], v[204:207], v[92:95]
	v_mfma_f32_16x16x32_bf16 v[80:83], v[146:149], v[212:215], v[80:83]
	v_mfma_f32_16x16x32_bf16 v[76:79], v[154:157], v[212:215], v[76:79]
	v_mfma_f32_16x16x32_bf16 v[128:131], v[150:153], v[182:185], v[128:131]
	v_mfma_f32_16x16x32_bf16 v[124:127], v[158:161], v[182:185], v[124:127]
	v_mfma_f32_16x16x32_bf16 v[112:115], v[150:153], v[190:193], v[112:115]
	v_mfma_f32_16x16x32_bf16 v[108:111], v[158:161], v[190:193], v[108:111]
	v_mfma_f32_16x16x32_bf16 v[96:99], v[150:153], v[208:211], v[96:99]
	v_mfma_f32_16x16x32_bf16 v[92:95], v[158:161], v[208:211], v[92:95]
	v_mfma_f32_16x16x32_bf16 v[80:83], v[150:153], v[226:229], v[80:83]
	v_mfma_f32_16x16x32_bf16 v[76:79], v[158:161], v[226:229], v[76:79]
	s_nop 0
	s_nop 0
	v_mfma_f32_16x16x32_bf16 v[120:123], v[162:165], v[178:181], v[120:123]
	v_mfma_f32_16x16x32_bf16 v[116:119], v[170:173], v[178:181], v[116:119]
	v_mfma_f32_16x16x32_bf16 v[104:107], v[162:165], v[186:189], v[104:107]
	v_mfma_f32_16x16x32_bf16 v[100:103], v[170:173], v[186:189], v[100:103]
	v_mfma_f32_16x16x32_bf16 v[88:91], v[162:165], v[204:207], v[88:91]
	v_mfma_f32_16x16x32_bf16 v[84:87], v[170:173], v[204:207], v[84:87]
	v_mfma_f32_16x16x32_bf16 v[72:75], v[162:165], v[212:215], v[72:75]
	v_mfma_f32_16x16x32_bf16 v[68:71], v[170:173], v[212:215], v[68:71]
	v_mfma_f32_16x16x32_bf16 v[120:123], v[166:169], v[182:185], v[120:123]
	v_mfma_f32_16x16x32_bf16 v[116:119], v[174:177], v[182:185], v[116:119]
	v_mfma_f32_16x16x32_bf16 v[104:107], v[166:169], v[190:193], v[104:107]
	v_mfma_f32_16x16x32_bf16 v[100:103], v[174:177], v[190:193], v[100:103]
	v_mfma_f32_16x16x32_bf16 v[88:91], v[166:169], v[208:211], v[88:91]
	v_mfma_f32_16x16x32_bf16 v[84:87], v[174:177], v[208:211], v[84:87]
	v_mfma_f32_16x16x32_bf16 v[72:75], v[166:169], v[226:229], v[72:75]
	v_mfma_f32_16x16x32_bf16 v[68:71], v[174:177], v[226:229], v[68:71]
	s_nop 0
	s_barrier
	s_add_i32 s49, s49, s31
	v_lshl_add_u64 v[194:195], s[20:21], 0, v[134:135]
	s_mov_b32 m0, s49
	ds_read_b128 v[178:181], v133 offset:16384
	ds_read_b128 v[182:185], v133 offset:17408
	ds_read_b128 v[186:189], v133 offset:18432
	ds_read_b128 v[190:193], v133 offset:19456
	ds_read_b128 v[204:207], v133 offset:20480
	ds_read_b128 v[208:211], v133 offset:21504
	ds_read_b128 v[212:215], v133 offset:22528
	ds_read_b128 v[226:229], v133 offset:23552
	global_load_lds_dwordx4 v[194:195], off
	s_add_i32 m0, s49, 0x2000
	s_add_u32 s58, s20, 0x80000
	v_lshl_add_u64 v[230:231], s[20:21], 0, v[138:139]
	s_addc_u32 s59, s21, 0
	s_add_i32 s49, s60, s31
	global_load_lds_dwordx4 v[230:231], off
	v_lshl_add_u64 v[232:233], s[58:59], 0, v[134:135]
	s_mov_b32 m0, s49
	v_lshl_add_u64 v[234:235], s[22:23], 0, v[140:141]
	global_load_lds_dwordx4 v[232:233], off
	v_lshl_add_u64 v[232:233], s[58:59], 0, v[138:139]
	s_add_i32 m0, s49, 0x2000
	s_nop 0
	global_load_lds_dwordx4 v[232:233], off
	v_lshl_add_u64 v[232:233], s[22:23], 0, v[136:137]
	s_mov_b32 m0, s34
	s_nop 0
	global_load_lds_dwordx4 v[232:233], off
	s_mov_b32 m0, s35
	s_nop 0
	global_load_lds_dwordx4 v[234:235], off
	s_waitcnt vmcnt(8)
	s_waitcnt lgkmcnt(0)
	s_barrier
	s_nop 0
	s_waitcnt lgkmcnt(0)
	v_mfma_f32_16x16x32_bf16 v[64:67], v[146:149], v[178:181], v[64:67]
	v_mfma_f32_16x16x32_bf16 v[60:63], v[154:157], v[178:181], v[60:63]
	v_mfma_f32_16x16x32_bf16 v[48:51], v[146:149], v[186:189], v[48:51]
	v_mfma_f32_16x16x32_bf16 v[44:47], v[154:157], v[186:189], v[44:47]
	v_mfma_f32_16x16x32_bf16 v[32:35], v[146:149], v[204:207], v[32:35]
	v_mfma_f32_16x16x32_bf16 v[28:31], v[154:157], v[204:207], v[28:31]
	v_mfma_f32_16x16x32_bf16 v[16:19], v[146:149], v[212:215], v[16:19]
	v_mfma_f32_16x16x32_bf16 v[12:15], v[154:157], v[212:215], v[12:15]
	v_mfma_f32_16x16x32_bf16 v[64:67], v[150:153], v[182:185], v[64:67]
	v_mfma_f32_16x16x32_bf16 v[60:63], v[158:161], v[182:185], v[60:63]
	v_mfma_f32_16x16x32_bf16 v[48:51], v[150:153], v[190:193], v[48:51]
	v_mfma_f32_16x16x32_bf16 v[44:47], v[158:161], v[190:193], v[44:47]
	v_mfma_f32_16x16x32_bf16 v[32:35], v[150:153], v[208:211], v[32:35]
	v_mfma_f32_16x16x32_bf16 v[28:31], v[158:161], v[208:211], v[28:31]
	v_mfma_f32_16x16x32_bf16 v[16:19], v[150:153], v[226:229], v[16:19]
	v_mfma_f32_16x16x32_bf16 v[12:15], v[158:161], v[226:229], v[12:15]
	s_nop 0
	s_nop 0
	v_mfma_f32_16x16x32_bf16 v[56:59], v[162:165], v[178:181], v[56:59]
	v_mfma_f32_16x16x32_bf16 v[52:55], v[170:173], v[178:181], v[52:55]
	v_mfma_f32_16x16x32_bf16 v[40:43], v[162:165], v[186:189], v[40:43]
	v_mfma_f32_16x16x32_bf16 v[36:39], v[170:173], v[186:189], v[36:39]
	v_mfma_f32_16x16x32_bf16 v[24:27], v[162:165], v[204:207], v[24:27]
	v_mfma_f32_16x16x32_bf16 v[20:23], v[170:173], v[204:207], v[20:23]
	v_mfma_f32_16x16x32_bf16 v[8:11], v[162:165], v[212:215], v[8:11]
	v_mfma_f32_16x16x32_bf16 v[4:7], v[170:173], v[212:215], v[4:7]
	v_mfma_f32_16x16x32_bf16 v[56:59], v[166:169], v[182:185], v[56:59]
	v_mfma_f32_16x16x32_bf16 v[52:55], v[174:177], v[182:185], v[52:55]
	v_mfma_f32_16x16x32_bf16 v[40:43], v[166:169], v[190:193], v[40:43]
	v_mfma_f32_16x16x32_bf16 v[36:39], v[174:177], v[190:193], v[36:39]
	v_mfma_f32_16x16x32_bf16 v[24:27], v[166:169], v[208:211], v[24:27]
	v_mfma_f32_16x16x32_bf16 v[20:23], v[174:177], v[208:211], v[20:23]
	v_mfma_f32_16x16x32_bf16 v[8:11], v[166:169], v[226:229], v[8:11]
	v_mfma_f32_16x16x32_bf16 v[4:7], v[174:177], v[226:229], v[4:7]
	s_nop 0
	s_barrier
	s_add_i32 s49, 0, 0x18000
	v_add_u32_e32 v2, s49, v1
	s_add_i32 s58, 0, 0x1c000
	ds_read_b128 v[146:149], v2
	ds_read_b128 v[150:153], v2 offset:1024
	ds_read_b128 v[154:157], v2 offset:2048
	ds_read_b128 v[158:161], v2 offset:3072
	v_add_u32_e32 v2, s58, v1
	ds_read_b128 v[162:165], v2
	ds_read_b128 v[166:169], v2 offset:1024
	ds_read_b128 v[170:173], v2 offset:2048
	ds_read_b128 v[174:177], v2 offset:3072
	s_add_u32 s22, s22, 0x80000
	s_addc_u32 s23, s23, 0
	s_mov_b32 m0, s36
	v_lshl_add_u64 v[236:237], s[22:23], 0, v[136:137]
	ds_read_b128 v[178:181], v133 offset:32768
	ds_read_b128 v[182:185], v133 offset:33792
	ds_read_b128 v[186:189], v133 offset:34816
	ds_read_b128 v[190:193], v133 offset:35840
	ds_read_b128 v[204:207], v133 offset:36864
	ds_read_b128 v[208:211], v133 offset:37888
	ds_read_b128 v[212:215], v133 offset:38912
	ds_read_b128 v[226:229], v133 offset:39936
	global_load_lds_dwordx4 v[236:237], off
	v_lshl_add_u64 v[236:237], s[22:23], 0, v[140:141]
	s_mov_b32 m0, s37
	s_nop 0
	global_load_lds_dwordx4 v[236:237], off
	s_waitcnt vmcnt(8)
	s_waitcnt lgkmcnt(0)
	s_barrier
	s_nop 0
	s_waitcnt lgkmcnt(0)
	v_mfma_f32_16x16x32_bf16 v[128:131], v[146:149], v[178:181], v[128:131]
	v_mfma_f32_16x16x32_bf16 v[124:127], v[154:157], v[178:181], v[124:127]
	v_mfma_f32_16x16x32_bf16 v[112:115], v[146:149], v[186:189], v[112:115]
	v_mfma_f32_16x16x32_bf16 v[108:111], v[154:157], v[186:189], v[108:111]
	v_mfma_f32_16x16x32_bf16 v[96:99], v[146:149], v[204:207], v[96:99]
	v_mfma_f32_16x16x32_bf16 v[92:95], v[154:157], v[204:207], v[92:95]
	v_mfma_f32_16x16x32_bf16 v[80:83], v[146:149], v[212:215], v[80:83]
	v_mfma_f32_16x16x32_bf16 v[76:79], v[154:157], v[212:215], v[76:79]
	v_mfma_f32_16x16x32_bf16 v[128:131], v[150:153], v[182:185], v[128:131]
	v_mfma_f32_16x16x32_bf16 v[124:127], v[158:161], v[182:185], v[124:127]
	v_mfma_f32_16x16x32_bf16 v[112:115], v[150:153], v[190:193], v[112:115]
	v_mfma_f32_16x16x32_bf16 v[108:111], v[158:161], v[190:193], v[108:111]
	v_mfma_f32_16x16x32_bf16 v[96:99], v[150:153], v[208:211], v[96:99]
	v_mfma_f32_16x16x32_bf16 v[92:95], v[158:161], v[208:211], v[92:95]
	v_mfma_f32_16x16x32_bf16 v[80:83], v[150:153], v[226:229], v[80:83]
	v_mfma_f32_16x16x32_bf16 v[76:79], v[158:161], v[226:229], v[76:79]
	s_nop 0
	s_nop 0
	v_mfma_f32_16x16x32_bf16 v[120:123], v[162:165], v[178:181], v[120:123]
	v_mfma_f32_16x16x32_bf16 v[116:119], v[170:173], v[178:181], v[116:119]
	v_mfma_f32_16x16x32_bf16 v[104:107], v[162:165], v[186:189], v[104:107]
	v_mfma_f32_16x16x32_bf16 v[100:103], v[170:173], v[186:189], v[100:103]
	v_mfma_f32_16x16x32_bf16 v[88:91], v[162:165], v[204:207], v[88:91]
	v_mfma_f32_16x16x32_bf16 v[84:87], v[170:173], v[204:207], v[84:87]
	v_mfma_f32_16x16x32_bf16 v[72:75], v[162:165], v[212:215], v[72:75]
	v_mfma_f32_16x16x32_bf16 v[68:71], v[170:173], v[212:215], v[68:71]
	v_mfma_f32_16x16x32_bf16 v[120:123], v[166:169], v[182:185], v[120:123]
	v_mfma_f32_16x16x32_bf16 v[116:119], v[174:177], v[182:185], v[116:119]
	v_mfma_f32_16x16x32_bf16 v[104:107], v[166:169], v[190:193], v[104:107]
	v_mfma_f32_16x16x32_bf16 v[100:103], v[174:177], v[190:193], v[100:103]
	v_mfma_f32_16x16x32_bf16 v[88:91], v[166:169], v[208:211], v[88:91]
	v_mfma_f32_16x16x32_bf16 v[84:87], v[174:177], v[208:211], v[84:87]
	v_mfma_f32_16x16x32_bf16 v[72:75], v[166:169], v[226:229], v[72:75]
	v_mfma_f32_16x16x32_bf16 v[68:71], v[174:177], v[226:229], v[68:71]
	s_nop 0
	s_barrier
	s_add_i32 s22, s49, s31
	v_lshl_add_u64 v[194:195], v[194:195], 0, s[94:95]
	s_mov_b32 m0, s22
	ds_read_b128 v[178:181], v133 offset:49152
	ds_read_b128 v[182:185], v133 offset:50176
	ds_read_b128 v[186:189], v133 offset:51200
	ds_read_b128 v[190:193], v133 offset:52224
	ds_read_b128 v[204:207], v133 offset:53248
	ds_read_b128 v[208:211], v133 offset:54272
	ds_read_b128 v[212:215], v133 offset:55296
	ds_read_b128 v[226:229], v133 offset:56320
	global_load_lds_dwordx4 v[194:195], off
	s_add_i32 m0, s22, 0x2000
	s_add_u32 s20, s20, 0x80080
	v_lshl_add_u64 v[194:195], v[230:231], 0, s[94:95]
	s_addc_u32 s21, s21, 0
	s_add_i32 s22, s58, s31
	global_load_lds_dwordx4 v[194:195], off
	v_lshl_add_u64 v[194:195], s[20:21], 0, v[134:135]
	s_mov_b32 m0, s22
	s_nop 0
	global_load_lds_dwordx4 v[194:195], off
	v_lshl_add_u64 v[194:195], s[20:21], 0, v[138:139]
	s_add_i32 m0, s22, 0x2000
	s_nop 0
	global_load_lds_dwordx4 v[194:195], off
	v_lshl_add_u64 v[194:195], v[232:233], 0, s[94:95]
	s_mov_b32 m0, s40
	s_nop 0
	global_load_lds_dwordx4 v[194:195], off
	v_lshl_add_u64 v[194:195], v[234:235], 0, s[94:95]
	s_mov_b32 m0, s41
	s_nop 0
	global_load_lds_dwordx4 v[194:195], off
	s_waitcnt vmcnt(8)
	s_waitcnt lgkmcnt(0)
	s_barrier
	s_nop 0
	s_waitcnt lgkmcnt(0)
	v_mfma_f32_16x16x32_bf16 v[64:67], v[146:149], v[178:181], v[64:67]
	v_mfma_f32_16x16x32_bf16 v[60:63], v[154:157], v[178:181], v[60:63]
	v_mfma_f32_16x16x32_bf16 v[48:51], v[146:149], v[186:189], v[48:51]
	v_mfma_f32_16x16x32_bf16 v[44:47], v[154:157], v[186:189], v[44:47]
	v_mfma_f32_16x16x32_bf16 v[32:35], v[146:149], v[204:207], v[32:35]
	v_mfma_f32_16x16x32_bf16 v[28:31], v[154:157], v[204:207], v[28:31]
	v_mfma_f32_16x16x32_bf16 v[16:19], v[146:149], v[212:215], v[16:19]
	v_mfma_f32_16x16x32_bf16 v[12:15], v[154:157], v[212:215], v[12:15]
	v_mfma_f32_16x16x32_bf16 v[64:67], v[150:153], v[182:185], v[64:67]
	v_mfma_f32_16x16x32_bf16 v[60:63], v[158:161], v[182:185], v[60:63]
	v_mfma_f32_16x16x32_bf16 v[48:51], v[150:153], v[190:193], v[48:51]
	v_mfma_f32_16x16x32_bf16 v[44:47], v[158:161], v[190:193], v[44:47]
	v_mfma_f32_16x16x32_bf16 v[32:35], v[150:153], v[208:211], v[32:35]
	v_mfma_f32_16x16x32_bf16 v[28:31], v[158:161], v[208:211], v[28:31]
	v_mfma_f32_16x16x32_bf16 v[16:19], v[150:153], v[226:229], v[16:19]
	v_mfma_f32_16x16x32_bf16 v[12:15], v[158:161], v[226:229], v[12:15]
	s_nop 0
	s_nop 0
	v_mfma_f32_16x16x32_bf16 v[56:59], v[162:165], v[178:181], v[56:59]
	v_mfma_f32_16x16x32_bf16 v[52:55], v[170:173], v[178:181], v[52:55]
	v_mfma_f32_16x16x32_bf16 v[40:43], v[162:165], v[186:189], v[40:43]
	v_mfma_f32_16x16x32_bf16 v[36:39], v[170:173], v[186:189], v[36:39]
	v_mfma_f32_16x16x32_bf16 v[24:27], v[162:165], v[204:207], v[24:27]
	v_mfma_f32_16x16x32_bf16 v[20:23], v[170:173], v[204:207], v[20:23]
	v_mfma_f32_16x16x32_bf16 v[8:11], v[162:165], v[212:215], v[8:11]
	v_mfma_f32_16x16x32_bf16 v[4:7], v[170:173], v[212:215], v[4:7]
	v_mfma_f32_16x16x32_bf16 v[56:59], v[166:169], v[182:185], v[56:59]
	v_mfma_f32_16x16x32_bf16 v[52:55], v[174:177], v[182:185], v[52:55]
	v_mfma_f32_16x16x32_bf16 v[40:43], v[166:169], v[190:193], v[40:43]
	v_mfma_f32_16x16x32_bf16 v[36:39], v[174:177], v[190:193], v[36:39]
	v_mfma_f32_16x16x32_bf16 v[24:27], v[166:169], v[208:211], v[24:27]
	v_mfma_f32_16x16x32_bf16 v[20:23], v[174:177], v[208:211], v[20:23]
	v_mfma_f32_16x16x32_bf16 v[8:11], v[166:169], v[226:229], v[8:11]
	v_mfma_f32_16x16x32_bf16 v[4:7], v[174:177], v[226:229], v[4:7]
	s_nop 0
	s_barrier
	s_add_i32 s48, s48, 2
	s_add_u32 s3, s3, 0x100
	s_addc_u32 s46, s46, 0
	s_add_u32 s18, s18, 0x100
	s_addc_u32 s19, s19, 0
	s_cmp_gt_u32 s48, 29
	s_cbranch_scc0 .LBB0_198
	s_and_b64 vcc, exec, s[10:11]
	s_cbranch_vccz .LBB0_201
	s_barrier

.LBB0_223:
	s_andn2_b64 vcc, exec, s[6:7]
	s_cbranch_vccnz .LBB0_259
	v_bfe_i32 v5, v1, 27, 1
	v_lshlrev_b32_e32 v4, 4, v1
	v_lshrrev_b32_e32 v5, 22, v5
	v_add_u32_e32 v5, v4, v5
	v_and_b32_e32 v5, 0xfffffc00, v5
	v_sub_u32_e32 v5, v4, v5
	v_lshrrev_b32_e32 v6, 4, v5
	v_ashrrev_i32_e32 v2, 31, v1
	v_bitop3_b32 v5, v6, v5, 32 bitop3:0x6c
	v_lshrrev_b32_e32 v2, 26, v2
	v_ashrrev_i32_e32 v7, 31, v5
	v_add_u32_e32 v2, v1, v2
	v_lshrrev_b32_e32 v7, 26, v7
	v_ashrrev_i32_e32 v2, 6, v2
	v_add_u32_e32 v7, v5, v7
	v_lshlrev_b32_e32 v6, 3, v2
	v_ashrrev_i32_e32 v12, 6, v7
	v_and_b32_e32 v7, 0xc0, v7
	v_and_b32_e32 v6, -16, v6
	v_sub_u32_e32 v5, v5, v7
	v_add_u32_e32 v6, v12, v6
	v_ashrrev_i16_sdwa v5, v216, sext(v5) dst_sel:DWORD dst_unused:UNUSED_PAD src0_sel:DWORD src1_sel:BYTE_0
	v_lshlrev_b32_e32 v8, 5, v2
	v_bfe_i32 v13, v5, 0, 16
	v_lshlrev_b32_e32 v5, 1, v6
	v_lshrrev_b32_e32 v7, 2, v6
	v_and_b32_e32 v9, 3, v12
	s_mov_b32 s0, 0xfffe0
	v_and_b32_e32 v8, 32, v8
	v_and_b32_e32 v5, 24, v5
	v_and_b32_e32 v7, 4, v7
	v_and_or_b32 v9, v6, s0, v9
	v_or3_b32 v5, v9, v7, v5
	v_add_lshl_u32 v7, v8, v13, 1
	v_add_u32_e32 v4, 0x2000, v4
	v_lshl_add_u32 v134, v5, 12, v7
	v_ashrrev_i32_e32 v5, 31, v4
	v_lshrrev_b32_e32 v5, 22, v5
	v_add_u32_e32 v5, v4, v5
	v_ashrrev_i32_e32 v14, 10, v5
	v_mul_i32_i24_e32 v5, 0x400, v14
	v_sub_u32_e32 v4, v4, v5
	v_lshrrev_b32_e32 v5, 4, v4
	v_bitop3_b32 v4, v5, v4, 32 bitop3:0x6c
	v_lshl_add_u32 v136, v6, 12, v7
	v_ashrrev_i32_e32 v6, 31, v4
	v_lshrrev_b32_e32 v6, 26, v6
	v_add_u32_e32 v6, v4, v6
	v_lshlrev_b32_e32 v5, 3, v14
	v_ashrrev_i32_e32 v15, 6, v6
	v_and_b32_e32 v6, 0xc0, v6
	s_ashr_i32 s10, s3, 6
	v_and_b32_e32 v5, -16, v5
	v_sub_u32_e32 v4, v4, v6
	v_add_u32_e32 v5, v15, v5
	v_ashrrev_i16_sdwa v4, v216, sext(v4) dst_sel:DWORD dst_unused:UNUSED_PAD src0_sel:DWORD src1_sel:BYTE_0
	s_lshl_b32 s34, s10, 10
	v_lshlrev_b32_e32 v7, 5, v14
	v_bfe_i32 v16, v4, 0, 16
	v_lshlrev_b32_e32 v4, 1, v5
	v_lshrrev_b32_e32 v6, 2, v5
	v_and_b32_e32 v8, 3, v15
	s_add_i32 s35, s34, 0
	v_and_b32_e32 v7, 32, v7
	v_and_b32_e32 v4, 24, v4
	v_and_b32_e32 v6, 4, v6
	v_and_or_b32 v8, v5, s0, v8
	s_waitcnt lgkmcnt(0)
	s_add_i32 m0, s35, 0x10000
	v_or3_b32 v4, v8, v6, v4
	v_add_lshl_u32 v6, v7, v16, 1
	s_ashr_i32 s11, s3, 8
	global_load_lds_dwordx4 v134, s[20:21]
	s_add_i32 m0, s35, 0x12000
	v_lshl_add_u32 v138, v4, 12, v6
	s_add_u32 s6, s20, 0x80000
	global_load_lds_dwordx4 v138, s[20:21]
	s_addc_u32 s7, s21, 0
	s_add_i32 m0, s35, 0x14000
	s_add_i32 s36, s35, 0x2000
	global_load_lds_dwordx4 v134, s[6:7]
	s_add_i32 m0, s35, 0x16000
	v_lshl_add_u32 v140, v5, 12, v6
	global_load_lds_dwordx4 v138, s[6:7]
	s_mov_b32 m0, s35
	s_add_u32 s6, s18, 0x80000
	global_load_lds_dwordx4 v136, s[18:19]
	s_mov_b32 m0, s36
	s_addc_u32 s7, s19, 0
	s_add_i32 s37, s35, 0x4000
	global_load_lds_dwordx4 v140, s[18:19]
	s_mov_b32 m0, s37
	s_add_i32 s38, s35, 0x6000
	global_load_lds_dwordx4 v136, s[6:7]
	s_mov_b32 m0, s38
	v_mov_b32_e32 v135, v3
	global_load_lds_dwordx4 v140, s[6:7]
	v_mov_b32_e32 v139, v3
	v_mov_b32_e32 v137, v3
	v_mov_b32_e32 v141, v3
	s_cmp_eq_u32 s11, 1
	v_lshl_add_u64 v[10:11], s[20:21], 0, v[134:135]
	v_lshl_add_u64 v[8:9], s[20:21], 0, v[138:139]
	v_lshl_add_u64 v[4:5], s[18:19], 0, v[136:137]
	s_cselect_b64 s[6:7], -1, 0
	s_cmp_lg_u32 s11, 1
	v_lshl_add_u64 v[6:7], s[18:19], 0, v[140:141]
	s_cbranch_scc1 .LBB0_226
	s_barrier
	s_setprio 1

.LBB0_236:
	s_add_u32 s20, s18, 0xfff80080
	s_addc_u32 s21, s19, -1
	s_add_i32 s58, 0, 0x10000
	s_cmp_eq_u32 s49, 28
	s_cselect_b32 s23, s15, s21
	s_cselect_b32 s22, s14, s20
	v_add_u32_e32 v2, s58, v1
	s_cselect_b32 s21, s17, s46
	s_cselect_b32 s20, s16, s3
	s_add_i32 s60, 0, 0x14000
	ds_read_b128 v[146:149], v2
	ds_read_b128 v[150:153], v2 offset:1024
	ds_read_b128 v[154:157], v2 offset:2048
	ds_read_b128 v[158:161], v2 offset:3072
	v_add_u32_e32 v2, s60, v1
	ds_read_b128 v[162:165], v2
	ds_read_b128 v[166:169], v2 offset:1024
	ds_read_b128 v[170:173], v2 offset:2048
	ds_read_b128 v[174:177], v2 offset:3072
	v_lshl_add_u64 v[194:195], s[18:19], 0, v[144:145]
	s_add_i32 m0, s35, 0xc000
	ds_read_b128 v[178:181], v133
	ds_read_b128 v[182:185], v133 offset:1024
	ds_read_b128 v[186:189], v133 offset:2048
	ds_read_b128 v[190:193], v133 offset:3072
	ds_read_b128 v[204:207], v133 offset:4096
	ds_read_b128 v[208:211], v133 offset:5120
	ds_read_b128 v[212:215], v133 offset:6144
	ds_read_b128 v[226:229], v133 offset:7168
	global_load_lds_dwordx4 v[194:195], off
	v_lshl_add_u64 v[194:195], s[18:19], 0, v[142:143]
	s_add_i32 m0, s35, 0xe000
	s_nop 0
	global_load_lds_dwordx4 v[194:195], off
	s_waitcnt vmcnt(8)
	s_waitcnt lgkmcnt(0)
	s_barrier
	s_nop 0
	s_waitcnt lgkmcnt(0)
	v_mfma_f32_16x16x32_bf16 v[128:131], v[146:149], v[178:181], v[128:131]
	v_mfma_f32_16x16x32_bf16 v[124:127], v[154:157], v[178:181], v[124:127]
	v_mfma_f32_16x16x32_bf16 v[112:115], v[146:149], v[186:189], v[112:115]
	v_mfma_f32_16x16x32_bf16 v[108:111], v[154:157], v[186:189], v[108:111]
	v_mfma_f32_16x16x32_bf16 v[96:99], v[146:149], v[204:207], v[96:99]
	v_mfma_f32_16x16x32_bf16 v[92:95], v[154:157], v[204:207], v[92:95]
	v_mfma_f32_16x16x32_bf16 v[80:83], v[146:149], v[212:215], v[80:83]
	v_mfma_f32_16x16x32_bf16 v[76:79], v[154:157], v[212:215], v[76:79]
	v_mfma_f32_16x16x32_bf16 v[128:131], v[150:153], v[182:185], v[128:131]
	v_mfma_f32_16x16x32_bf16 v[124:127], v[158:161], v[182:185], v[124:127]
	v_mfma_f32_16x16x32_bf16 v[112:115], v[150:153], v[190:193], v[112:115]
	v_mfma_f32_16x16x32_bf16 v[108:111], v[158:161], v[190:193], v[108:111]
	v_mfma_f32_16x16x32_bf16 v[96:99], v[150:153], v[208:211], v[96:99]
	v_mfma_f32_16x16x32_bf16 v[92:95], v[158:161], v[208:211], v[92:95]
	v_mfma_f32_16x16x32_bf16 v[80:83], v[150:153], v[226:229], v[80:83]
	v_mfma_f32_16x16x32_bf16 v[76:79], v[158:161], v[226:229], v[76:79]
	s_nop 0
	s_nop 0
	v_mfma_f32_16x16x32_bf16 v[120:123], v[162:165], v[178:181], v[120:123]
	v_mfma_f32_16x16x32_bf16 v[116:119], v[170:173], v[178:181], v[116:119]
	v_mfma_f32_16x16x32_bf16 v[104:107], v[162:165], v[186:189], v[104:107]
	v_mfma_f32_16x16x32_bf16 v[100:103], v[170:173], v[186:189], v[100:103]
	v_mfma_f32_16x16x32_bf16 v[88:91], v[162:165], v[204:207], v[88:91]
	v_mfma_f32_16x16x32_bf16 v[84:87], v[170:173], v[204:207], v[84:87]
	v_mfma_f32_16x16x32_bf16 v[72:75], v[162:165], v[212:215], v[72:75]
	v_mfma_f32_16x16x32_bf16 v[68:71], v[170:173], v[212:215], v[68:71]
	v_mfma_f32_16x16x32_bf16 v[120:123], v[166:169], v[182:185], v[120:123]
	v_mfma_f32_16x16x32_bf16 v[116:119], v[174:177], v[182:185], v[116:119]
	v_mfma_f32_16x16x32_bf16 v[104:107], v[166:169], v[190:193], v[104:107]
	v_mfma_f32_16x16x32_bf16 v[100:103], v[174:177], v[190:193], v[100:103]
	v_mfma_f32_16x16x32_bf16 v[88:91], v[166:169], v[208:211], v[88:91]
	v_mfma_f32_16x16x32_bf16 v[84:87], v[174:177], v[208:211], v[84:87]
	v_mfma_f32_16x16x32_bf16 v[72:75], v[166:169], v[226:229], v[72:75]
	v_mfma_f32_16x16x32_bf16 v[68:71], v[174:177], v[226:229], v[68:71]
	s_nop 0
	s_barrier
	s_add_i32 s58, s58, s34
	v_lshl_add_u64 v[194:195], s[20:21], 0, v[134:135]
	s_mov_b32 m0, s58
	ds_read_b128 v[178:181], v133 offset:16384
	ds_read_b128 v[182:185], v133 offset:17408
	ds_read_b128 v[186:189], v133 offset:18432
	ds_read_b128 v[190:193], v133 offset:19456
	ds_read_b128 v[204:207], v133 offset:20480
	ds_read_b128 v[208:211], v133 offset:21504
	ds_read_b128 v[212:215], v133 offset:22528
	ds_read_b128 v[226:229], v133 offset:23552
	global_load_lds_dwordx4 v[194:195], off
	s_add_i32 m0, s58, 0x2000
	s_add_u32 s58, s20, 0x80000
	v_lshl_add_u64 v[230:231], s[20:21], 0, v[138:139]
	s_addc_u32 s59, s21, 0
	s_add_i32 s60, s60, s34
	global_load_lds_dwordx4 v[230:231], off
	v_lshl_add_u64 v[232:233], s[58:59], 0, v[134:135]
	s_mov_b32 m0, s60
	v_lshl_add_u64 v[234:235], s[22:23], 0, v[140:141]
	global_load_lds_dwordx4 v[232:233], off
	v_lshl_add_u64 v[232:233], s[58:59], 0, v[138:139]
	s_add_i32 m0, s60, 0x2000
	s_nop 0
	global_load_lds_dwordx4 v[232:233], off
	v_lshl_add_u64 v[232:233], s[22:23], 0, v[136:137]
	s_mov_b32 m0, s35
	s_nop 0
	global_load_lds_dwordx4 v[232:233], off
	s_mov_b32 m0, s36
	s_nop 0
	global_load_lds_dwordx4 v[234:235], off
	s_waitcnt vmcnt(8)
	s_waitcnt lgkmcnt(0)
	s_barrier
	s_nop 0
	s_waitcnt lgkmcnt(0)
	v_mfma_f32_16x16x32_bf16 v[64:67], v[146:149], v[178:181], v[64:67]
	v_mfma_f32_16x16x32_bf16 v[60:63], v[154:157], v[178:181], v[60:63]
	v_mfma_f32_16x16x32_bf16 v[48:51], v[146:149], v[186:189], v[48:51]
	v_mfma_f32_16x16x32_bf16 v[44:47], v[154:157], v[186:189], v[44:47]
	v_mfma_f32_16x16x32_bf16 v[32:35], v[146:149], v[204:207], v[32:35]
	v_mfma_f32_16x16x32_bf16 v[28:31], v[154:157], v[204:207], v[28:31]
	v_mfma_f32_16x16x32_bf16 v[16:19], v[146:149], v[212:215], v[16:19]
	v_mfma_f32_16x16x32_bf16 v[12:15], v[154:157], v[212:215], v[12:15]
	v_mfma_f32_16x16x32_bf16 v[64:67], v[150:153], v[182:185], v[64:67]
	v_mfma_f32_16x16x32_bf16 v[60:63], v[158:161], v[182:185], v[60:63]
	v_mfma_f32_16x16x32_bf16 v[48:51], v[150:153], v[190:193], v[48:51]
	v_mfma_f32_16x16x32_bf16 v[44:47], v[158:161], v[190:193], v[44:47]
	v_mfma_f32_16x16x32_bf16 v[32:35], v[150:153], v[208:211], v[32:35]
	v_mfma_f32_16x16x32_bf16 v[28:31], v[158:161], v[208:211], v[28:31]
	v_mfma_f32_16x16x32_bf16 v[16:19], v[150:153], v[226:229], v[16:19]
	v_mfma_f32_16x16x32_bf16 v[12:15], v[158:161], v[226:229], v[12:15]
	s_nop 0
	s_nop 0
	v_mfma_f32_16x16x32_bf16 v[56:59], v[162:165], v[178:181], v[56:59]
	v_mfma_f32_16x16x32_bf16 v[52:55], v[170:173], v[178:181], v[52:55]
	v_mfma_f32_16x16x32_bf16 v[40:43], v[162:165], v[186:189], v[40:43]
	v_mfma_f32_16x16x32_bf16 v[36:39], v[170:173], v[186:189], v[36:39]
	v_mfma_f32_16x16x32_bf16 v[24:27], v[162:165], v[204:207], v[24:27]
	v_mfma_f32_16x16x32_bf16 v[20:23], v[170:173], v[204:207], v[20:23]
	v_mfma_f32_16x16x32_bf16 v[8:11], v[162:165], v[212:215], v[8:11]
	v_mfma_f32_16x16x32_bf16 v[4:7], v[170:173], v[212:215], v[4:7]
	v_mfma_f32_16x16x32_bf16 v[56:59], v[166:169], v[182:185], v[56:59]
	v_mfma_f32_16x16x32_bf16 v[52:55], v[174:177], v[182:185], v[52:55]
	v_mfma_f32_16x16x32_bf16 v[40:43], v[166:169], v[190:193], v[40:43]
	v_mfma_f32_16x16x32_bf16 v[36:39], v[174:177], v[190:193], v[36:39]
	v_mfma_f32_16x16x32_bf16 v[24:27], v[166:169], v[208:211], v[24:27]
	v_mfma_f32_16x16x32_bf16 v[20:23], v[174:177], v[208:211], v[20:23]
	v_mfma_f32_16x16x32_bf16 v[8:11], v[166:169], v[226:229], v[8:11]
	v_mfma_f32_16x16x32_bf16 v[4:7], v[174:177], v[226:229], v[4:7]
	s_nop 0
	s_barrier
	s_add_i32 s58, 0, 0x18000
	v_add_u32_e32 v2, s58, v1
	s_add_i32 s59, 0, 0x1c000
	ds_read_b128 v[146:149], v2
	ds_read_b128 v[150:153], v2 offset:1024
	ds_read_b128 v[154:157], v2 offset:2048
	ds_read_b128 v[158:161], v2 offset:3072
	v_add_u32_e32 v2, s59, v1
	ds_read_b128 v[162:165], v2
	ds_read_b128 v[166:169], v2 offset:1024
	ds_read_b128 v[170:173], v2 offset:2048
	ds_read_b128 v[174:177], v2 offset:3072
	s_add_u32 s22, s22, 0x80000
	s_addc_u32 s23, s23, 0
	s_mov_b32 m0, s37
	v_lshl_add_u64 v[236:237], s[22:23], 0, v[136:137]
	ds_read_b128 v[178:181], v133 offset:32768
	ds_read_b128 v[182:185], v133 offset:33792
	ds_read_b128 v[186:189], v133 offset:34816
	ds_read_b128 v[190:193], v133 offset:35840
	ds_read_b128 v[204:207], v133 offset:36864
	ds_read_b128 v[208:211], v133 offset:37888
	ds_read_b128 v[212:215], v133 offset:38912
	ds_read_b128 v[226:229], v133 offset:39936
	global_load_lds_dwordx4 v[236:237], off
	v_lshl_add_u64 v[236:237], s[22:23], 0, v[140:141]
	s_mov_b32 m0, s38
	s_nop 0
	global_load_lds_dwordx4 v[236:237], off
	s_waitcnt vmcnt(8)
	s_waitcnt lgkmcnt(0)
	s_barrier
	s_nop 0
	s_waitcnt lgkmcnt(0)
	v_mfma_f32_16x16x32_bf16 v[128:131], v[146:149], v[178:181], v[128:131]
	v_mfma_f32_16x16x32_bf16 v[124:127], v[154:157], v[178:181], v[124:127]
	v_mfma_f32_16x16x32_bf16 v[112:115], v[146:149], v[186:189], v[112:115]
	v_mfma_f32_16x16x32_bf16 v[108:111], v[154:157], v[186:189], v[108:111]
	v_mfma_f32_16x16x32_bf16 v[96:99], v[146:149], v[204:207], v[96:99]
	v_mfma_f32_16x16x32_bf16 v[92:95], v[154:157], v[204:207], v[92:95]
	v_mfma_f32_16x16x32_bf16 v[80:83], v[146:149], v[212:215], v[80:83]
	v_mfma_f32_16x16x32_bf16 v[76:79], v[154:157], v[212:215], v[76:79]
	v_mfma_f32_16x16x32_bf16 v[128:131], v[150:153], v[182:185], v[128:131]
	v_mfma_f32_16x16x32_bf16 v[124:127], v[158:161], v[182:185], v[124:127]
	v_mfma_f32_16x16x32_bf16 v[112:115], v[150:153], v[190:193], v[112:115]
	v_mfma_f32_16x16x32_bf16 v[108:111], v[158:161], v[190:193], v[108:111]
	v_mfma_f32_16x16x32_bf16 v[96:99], v[150:153], v[208:211], v[96:99]
	v_mfma_f32_16x16x32_bf16 v[92:95], v[158:161], v[208:211], v[92:95]
	v_mfma_f32_16x16x32_bf16 v[80:83], v[150:153], v[226:229], v[80:83]
	v_mfma_f32_16x16x32_bf16 v[76:79], v[158:161], v[226:229], v[76:79]
	s_nop 0
	s_nop 0
	v_mfma_f32_16x16x32_bf16 v[120:123], v[162:165], v[178:181], v[120:123]
	v_mfma_f32_16x16x32_bf16 v[116:119], v[170:173], v[178:181], v[116:119]
	v_mfma_f32_16x16x32_bf16 v[104:107], v[162:165], v[186:189], v[104:107]
	v_mfma_f32_16x16x32_bf16 v[100:103], v[170:173], v[186:189], v[100:103]
	v_mfma_f32_16x16x32_bf16 v[88:91], v[162:165], v[204:207], v[88:91]
	v_mfma_f32_16x16x32_bf16 v[84:87], v[170:173], v[204:207], v[84:87]
	v_mfma_f32_16x16x32_bf16 v[72:75], v[162:165], v[212:215], v[72:75]
	v_mfma_f32_16x16x32_bf16 v[68:71], v[170:173], v[212:215], v[68:71]
	v_mfma_f32_16x16x32_bf16 v[120:123], v[166:169], v[182:185], v[120:123]
	v_mfma_f32_16x16x32_bf16 v[116:119], v[174:177], v[182:185], v[116:119]
	v_mfma_f32_16x16x32_bf16 v[104:107], v[166:169], v[190:193], v[104:107]
	v_mfma_f32_16x16x32_bf16 v[100:103], v[174:177], v[190:193], v[100:103]
	v_mfma_f32_16x16x32_bf16 v[88:91], v[166:169], v[208:211], v[88:91]
	v_mfma_f32_16x16x32_bf16 v[84:87], v[174:177], v[208:211], v[84:87]
	v_mfma_f32_16x16x32_bf16 v[72:75], v[166:169], v[226:229], v[72:75]
	v_mfma_f32_16x16x32_bf16 v[68:71], v[174:177], v[226:229], v[68:71]
	s_nop 0
	s_barrier
	s_add_i32 s22, s58, s34
	v_lshl_add_u64 v[194:195], v[194:195], 0, s[94:95]
	s_mov_b32 m0, s22
	ds_read_b128 v[178:181], v133 offset:49152
	ds_read_b128 v[182:185], v133 offset:50176
	ds_read_b128 v[186:189], v133 offset:51200
	ds_read_b128 v[190:193], v133 offset:52224
	ds_read_b128 v[204:207], v133 offset:53248
	ds_read_b128 v[208:211], v133 offset:54272
	ds_read_b128 v[212:215], v133 offset:55296
	ds_read_b128 v[226:229], v133 offset:56320
	global_load_lds_dwordx4 v[194:195], off
	s_add_i32 m0, s22, 0x2000
	s_add_u32 s20, s20, 0x80080
	v_lshl_add_u64 v[194:195], v[230:231], 0, s[94:95]
	s_addc_u32 s21, s21, 0
	s_add_i32 s22, s59, s34
	global_load_lds_dwordx4 v[194:195], off
	v_lshl_add_u64 v[194:195], s[20:21], 0, v[134:135]
	s_mov_b32 m0, s22
	s_nop 0
	global_load_lds_dwordx4 v[194:195], off
	v_lshl_add_u64 v[194:195], s[20:21], 0, v[138:139]
	s_add_i32 m0, s22, 0x2000
	s_nop 0
	global_load_lds_dwordx4 v[194:195], off
	v_lshl_add_u64 v[194:195], v[232:233], 0, s[94:95]
	s_mov_b32 m0, s41
	s_nop 0
	global_load_lds_dwordx4 v[194:195], off
	v_lshl_add_u64 v[194:195], v[234:235], 0, s[94:95]
	s_mov_b32 m0, s42
	s_nop 0
	global_load_lds_dwordx4 v[194:195], off
	s_waitcnt vmcnt(8)
	s_waitcnt lgkmcnt(0)
	s_barrier
	s_nop 0
	s_waitcnt lgkmcnt(0)
	v_mfma_f32_16x16x32_bf16 v[64:67], v[146:149], v[178:181], v[64:67]
	v_mfma_f32_16x16x32_bf16 v[60:63], v[154:157], v[178:181], v[60:63]
	v_mfma_f32_16x16x32_bf16 v[48:51], v[146:149], v[186:189], v[48:51]
	v_mfma_f32_16x16x32_bf16 v[44:47], v[154:157], v[186:189], v[44:47]
	v_mfma_f32_16x16x32_bf16 v[32:35], v[146:149], v[204:207], v[32:35]
	v_mfma_f32_16x16x32_bf16 v[28:31], v[154:157], v[204:207], v[28:31]
	v_mfma_f32_16x16x32_bf16 v[16:19], v[146:149], v[212:215], v[16:19]
	v_mfma_f32_16x16x32_bf16 v[12:15], v[154:157], v[212:215], v[12:15]
	v_mfma_f32_16x16x32_bf16 v[64:67], v[150:153], v[182:185], v[64:67]
	v_mfma_f32_16x16x32_bf16 v[60:63], v[158:161], v[182:185], v[60:63]
	v_mfma_f32_16x16x32_bf16 v[48:51], v[150:153], v[190:193], v[48:51]
	v_mfma_f32_16x16x32_bf16 v[44:47], v[158:161], v[190:193], v[44:47]
	v_mfma_f32_16x16x32_bf16 v[32:35], v[150:153], v[208:211], v[32:35]
	v_mfma_f32_16x16x32_bf16 v[28:31], v[158:161], v[208:211], v[28:31]
	v_mfma_f32_16x16x32_bf16 v[16:19], v[150:153], v[226:229], v[16:19]
	v_mfma_f32_16x16x32_bf16 v[12:15], v[158:161], v[226:229], v[12:15]
	s_nop 0
	s_nop 0
	v_mfma_f32_16x16x32_bf16 v[56:59], v[162:165], v[178:181], v[56:59]
	v_mfma_f32_16x16x32_bf16 v[52:55], v[170:173], v[178:181], v[52:55]
	v_mfma_f32_16x16x32_bf16 v[40:43], v[162:165], v[186:189], v[40:43]
	v_mfma_f32_16x16x32_bf16 v[36:39], v[170:173], v[186:189], v[36:39]
	v_mfma_f32_16x16x32_bf16 v[24:27], v[162:165], v[204:207], v[24:27]
	v_mfma_f32_16x16x32_bf16 v[20:23], v[170:173], v[204:207], v[20:23]
	v_mfma_f32_16x16x32_bf16 v[8:11], v[162:165], v[212:215], v[8:11]
	v_mfma_f32_16x16x32_bf16 v[4:7], v[170:173], v[212:215], v[4:7]
	v_mfma_f32_16x16x32_bf16 v[56:59], v[166:169], v[182:185], v[56:59]
	v_mfma_f32_16x16x32_bf16 v[52:55], v[174:177], v[182:185], v[52:55]
	v_mfma_f32_16x16x32_bf16 v[40:43], v[166:169], v[190:193], v[40:43]
	v_mfma_f32_16x16x32_bf16 v[36:39], v[174:177], v[190:193], v[36:39]
	v_mfma_f32_16x16x32_bf16 v[24:27], v[166:169], v[208:211], v[24:27]
	v_mfma_f32_16x16x32_bf16 v[20:23], v[174:177], v[208:211], v[20:23]
	v_mfma_f32_16x16x32_bf16 v[8:11], v[166:169], v[226:229], v[8:11]
	v_mfma_f32_16x16x32_bf16 v[4:7], v[174:177], v[226:229], v[4:7]
	s_nop 0
	s_barrier
	s_add_i32 s49, s49, 2
	s_add_u32 s3, s3, 0x100
	s_addc_u32 s46, s46, 0
	s_add_u32 s18, s18, 0x100
	s_addc_u32 s19, s19, 0
	s_cmp_gt_u32 s49, 29
	s_cbranch_scc0 .LBB0_236
	s_and_b64 vcc, exec, s[10:11]
	s_cbranch_vccz .LBB0_239
	s_barrier

.LBB0_715:
	s_andn2_b64 vcc, exec, s[2:3]
	s_cbranch_vccnz .LBB0_747
	s_waitcnt vmcnt(0)
	v_bfe_i32 v5, v1, 27, 1
	v_lshlrev_b32_e32 v4, 4, v1
	v_lshrrev_b32_e32 v5, 22, v5
	v_add_u32_e32 v5, v4, v5
	v_and_b32_e32 v5, 0xfffffc00, v5
	v_sub_u32_e32 v5, v4, v5
	v_lshrrev_b32_e32 v6, 4, v5
	v_ashrrev_i32_e32 v2, 31, v1
	v_bitop3_b32 v5, v6, v5, 32 bitop3:0x6c
	v_lshrrev_b32_e32 v2, 26, v2
	v_ashrrev_i32_e32 v7, 31, v5
	v_add_u32_e32 v2, v1, v2
	v_lshrrev_b32_e32 v7, 26, v7
	v_ashrrev_i32_e32 v2, 6, v2
	v_add_u32_e32 v7, v5, v7
	v_lshlrev_b32_e32 v6, 3, v2
	v_ashrrev_i32_e32 v12, 6, v7
	v_and_b32_e32 v7, 0xc0, v7
	v_and_b32_e32 v6, -16, v6
	v_sub_u32_e32 v5, v5, v7
	v_add_u32_e32 v6, v12, v6
	v_ashrrev_i16_sdwa v5, v216, sext(v5) dst_sel:DWORD dst_unused:UNUSED_PAD src0_sel:DWORD src1_sel:BYTE_0
	v_lshlrev_b32_e32 v8, 5, v2
	v_bfe_i32 v13, v5, 0, 16
	v_lshlrev_b32_e32 v5, 1, v6
	v_lshrrev_b32_e32 v7, 2, v6
	v_and_b32_e32 v9, 3, v12
	s_mov_b32 s3, 0xfffe0
	v_and_b32_e32 v8, 32, v8
	v_and_b32_e32 v5, 24, v5
	v_and_b32_e32 v7, 4, v7
	v_and_or_b32 v9, v6, s3, v9
	v_or3_b32 v5, v9, v7, v5
	v_add_lshl_u32 v7, v8, v13, 1
	v_add_u32_e32 v4, 0x2000, v4
	v_lshl_add_u32 v132, v5, 12, v7
	v_ashrrev_i32_e32 v5, 31, v4
	v_lshrrev_b32_e32 v5, 22, v5
	v_add_u32_e32 v5, v4, v5
	v_ashrrev_i32_e32 v14, 10, v5
	v_mul_i32_i24_e32 v5, 0x400, v14
	v_sub_u32_e32 v4, v4, v5
	v_lshrrev_b32_e32 v5, 4, v4
	v_bitop3_b32 v4, v5, v4, 32 bitop3:0x6c
	v_lshl_add_u32 v134, v6, 12, v7
	v_ashrrev_i32_e32 v6, 31, v4
	v_lshrrev_b32_e32 v6, 26, v6
	v_add_u32_e32 v6, v4, v6
	v_lshlrev_b32_e32 v5, 3, v14
	v_ashrrev_i32_e32 v15, 6, v6
	v_and_b32_e32 v6, 0xc0, v6
	s_ashr_i32 s2, s7, 6
	v_and_b32_e32 v5, -16, v5
	v_sub_u32_e32 v4, v4, v6
	v_add_u32_e32 v5, v15, v5
	v_ashrrev_i16_sdwa v4, v216, sext(v4) dst_sel:DWORD dst_unused:UNUSED_PAD src0_sel:DWORD src1_sel:BYTE_0
	s_lshl_b32 s27, s2, 10
	v_lshlrev_b32_e32 v7, 5, v14
	v_bfe_i32 v16, v4, 0, 16
	v_lshlrev_b32_e32 v4, 1, v5
	v_lshrrev_b32_e32 v6, 2, v5
	v_and_b32_e32 v8, 3, v15
	s_add_i32 s28, s27, 0
	v_and_b32_e32 v7, 32, v7
	v_and_b32_e32 v4, 24, v4
	v_and_b32_e32 v6, 4, v6
	v_and_or_b32 v8, v5, s3, v8
	s_waitcnt lgkmcnt(0)
	s_add_i32 m0, s28, 0x10000
	v_or3_b32 v4, v8, v6, v4
	v_add_lshl_u32 v6, v7, v16, 1
	s_ashr_i32 s3, s7, 8
	global_load_lds_dwordx4 v132, s[18:19]
	s_add_i32 m0, s28, 0x12000
	v_lshl_add_u32 v136, v4, 12, v6
	s_add_u32 s8, s18, 0x80000
	global_load_lds_dwordx4 v136, s[18:19]
	s_addc_u32 s9, s19, 0
	s_add_i32 m0, s28, 0x14000
	s_add_i32 s29, s28, 0x2000
	global_load_lds_dwordx4 v132, s[8:9]
	s_add_i32 m0, s28, 0x16000
	v_lshl_add_u32 v138, v5, 12, v6
	global_load_lds_dwordx4 v136, s[8:9]
	s_mov_b32 m0, s28
	s_add_u32 s8, s16, 0x80000
	global_load_lds_dwordx4 v134, s[16:17]
	s_mov_b32 m0, s29
	s_addc_u32 s9, s17, 0
	s_add_i32 s30, s28, 0x4000
	global_load_lds_dwordx4 v138, s[16:17]
	s_mov_b32 m0, s30
	s_add_i32 s31, s28, 0x6000
	global_load_lds_dwordx4 v134, s[8:9]
	s_mov_b32 m0, s31
	v_mov_b32_e32 v133, v3
	global_load_lds_dwordx4 v138, s[8:9]
	v_mov_b32_e32 v137, v3
	v_mov_b32_e32 v135, v3
	v_mov_b32_e32 v139, v3
	s_cmp_eq_u32 s3, 1
	v_lshl_add_u64 v[10:11], s[18:19], 0, v[132:133]
	v_lshl_add_u64 v[8:9], s[18:19], 0, v[136:137]
	v_lshl_add_u64 v[4:5], s[16:17], 0, v[134:135]
	s_cselect_b64 s[8:9], -1, 0
	s_cmp_lg_u32 s3, 1
	v_lshl_add_u64 v[6:7], s[16:17], 0, v[138:139]
	s_cbranch_scc1 .LBB0_718
	s_barrier
	s_setprio 1

.LBB0_724:
	s_add_u32 s18, s16, 0xfff80080
	s_addc_u32 s19, s17, -1
	s_add_i32 s44, 0, 0x10000
	s_cmp_eq_u32 s43, 28
	s_cselect_b32 s21, s13, s19
	s_cselect_b32 s20, s12, s18
	v_add_u32_e32 v2, s44, v1
	s_cselect_b32 s19, s15, s42
	s_cselect_b32 s18, s14, s7
	s_add_i32 s46, 0, 0x14000
	ds_read_b128 v[146:149], v2
	ds_read_b128 v[150:153], v2 offset:1024
	ds_read_b128 v[154:157], v2 offset:2048
	ds_read_b128 v[158:161], v2 offset:3072
	v_add_u32_e32 v2, s46, v1
	ds_read_b128 v[162:165], v2
	ds_read_b128 v[166:169], v2 offset:1024
	ds_read_b128 v[170:173], v2 offset:2048
	ds_read_b128 v[174:177], v2 offset:3072
	v_lshl_add_u64 v[194:195], s[16:17], 0, v[142:143]
	s_add_i32 m0, s28, 0xc000
	ds_read_b128 v[178:181], v144
	ds_read_b128 v[182:185], v144 offset:1024
	ds_read_b128 v[186:189], v144 offset:2048
	ds_read_b128 v[190:193], v144 offset:3072
	ds_read_b128 v[204:207], v144 offset:4096
	ds_read_b128 v[208:211], v144 offset:5120
	ds_read_b128 v[212:215], v144 offset:6144
	ds_read_b128 v[226:229], v144 offset:7168
	global_load_lds_dwordx4 v[194:195], off
	v_lshl_add_u64 v[194:195], s[16:17], 0, v[140:141]
	s_add_i32 m0, s28, 0xe000
	s_nop 0
	global_load_lds_dwordx4 v[194:195], off
	s_waitcnt vmcnt(8)
	s_waitcnt lgkmcnt(0)
	s_barrier
	s_nop 0
	s_waitcnt lgkmcnt(0)
	v_mfma_f32_16x16x32_bf16 v[128:131], v[146:149], v[178:181], v[128:131]
	v_mfma_f32_16x16x32_bf16 v[124:127], v[154:157], v[178:181], v[124:127]
	v_mfma_f32_16x16x32_bf16 v[112:115], v[146:149], v[186:189], v[112:115]
	v_mfma_f32_16x16x32_bf16 v[108:111], v[154:157], v[186:189], v[108:111]
	v_mfma_f32_16x16x32_bf16 v[96:99], v[146:149], v[204:207], v[96:99]
	v_mfma_f32_16x16x32_bf16 v[92:95], v[154:157], v[204:207], v[92:95]
	v_mfma_f32_16x16x32_bf16 v[80:83], v[146:149], v[212:215], v[80:83]
	v_mfma_f32_16x16x32_bf16 v[76:79], v[154:157], v[212:215], v[76:79]
	v_mfma_f32_16x16x32_bf16 v[128:131], v[150:153], v[182:185], v[128:131]
	v_mfma_f32_16x16x32_bf16 v[124:127], v[158:161], v[182:185], v[124:127]
	v_mfma_f32_16x16x32_bf16 v[112:115], v[150:153], v[190:193], v[112:115]
	v_mfma_f32_16x16x32_bf16 v[108:111], v[158:161], v[190:193], v[108:111]
	v_mfma_f32_16x16x32_bf16 v[96:99], v[150:153], v[208:211], v[96:99]
	v_mfma_f32_16x16x32_bf16 v[92:95], v[158:161], v[208:211], v[92:95]
	v_mfma_f32_16x16x32_bf16 v[80:83], v[150:153], v[226:229], v[80:83]
	v_mfma_f32_16x16x32_bf16 v[76:79], v[158:161], v[226:229], v[76:79]
	s_nop 0
	s_nop 0
	v_mfma_f32_16x16x32_bf16 v[120:123], v[162:165], v[178:181], v[120:123]
	v_mfma_f32_16x16x32_bf16 v[116:119], v[170:173], v[178:181], v[116:119]
	v_mfma_f32_16x16x32_bf16 v[104:107], v[162:165], v[186:189], v[104:107]
	v_mfma_f32_16x16x32_bf16 v[100:103], v[170:173], v[186:189], v[100:103]
	v_mfma_f32_16x16x32_bf16 v[88:91], v[162:165], v[204:207], v[88:91]
	v_mfma_f32_16x16x32_bf16 v[84:87], v[170:173], v[204:207], v[84:87]
	v_mfma_f32_16x16x32_bf16 v[72:75], v[162:165], v[212:215], v[72:75]
	v_mfma_f32_16x16x32_bf16 v[68:71], v[170:173], v[212:215], v[68:71]
	v_mfma_f32_16x16x32_bf16 v[120:123], v[166:169], v[182:185], v[120:123]
	v_mfma_f32_16x16x32_bf16 v[116:119], v[174:177], v[182:185], v[116:119]
	v_mfma_f32_16x16x32_bf16 v[104:107], v[166:169], v[190:193], v[104:107]
	v_mfma_f32_16x16x32_bf16 v[100:103], v[174:177], v[190:193], v[100:103]
	v_mfma_f32_16x16x32_bf16 v[88:91], v[166:169], v[208:211], v[88:91]
	v_mfma_f32_16x16x32_bf16 v[84:87], v[174:177], v[208:211], v[84:87]
	v_mfma_f32_16x16x32_bf16 v[72:75], v[166:169], v[226:229], v[72:75]
	v_mfma_f32_16x16x32_bf16 v[68:71], v[174:177], v[226:229], v[68:71]
	s_nop 0
	s_barrier
	s_add_i32 s44, s44, s27
	v_lshl_add_u64 v[194:195], s[18:19], 0, v[132:133]
	s_mov_b32 m0, s44
	ds_read_b128 v[178:181], v144 offset:16384
	ds_read_b128 v[182:185], v144 offset:17408
	ds_read_b128 v[186:189], v144 offset:18432
	ds_read_b128 v[190:193], v144 offset:19456
	ds_read_b128 v[204:207], v144 offset:20480
	ds_read_b128 v[208:211], v144 offset:21504
	ds_read_b128 v[212:215], v144 offset:22528
	ds_read_b128 v[226:229], v144 offset:23552
	global_load_lds_dwordx4 v[194:195], off
	s_add_i32 m0, s44, 0x2000
	s_add_u32 s44, s18, 0x80000
	v_lshl_add_u64 v[230:231], s[18:19], 0, v[136:137]
	s_addc_u32 s45, s19, 0
	s_add_i32 s46, s46, s27
	global_load_lds_dwordx4 v[230:231], off
	v_lshl_add_u64 v[232:233], s[44:45], 0, v[132:133]
	s_mov_b32 m0, s46
	v_lshl_add_u64 v[234:235], s[20:21], 0, v[138:139]
	global_load_lds_dwordx4 v[232:233], off
	v_lshl_add_u64 v[232:233], s[44:45], 0, v[136:137]
	s_add_i32 m0, s46, 0x2000
	s_nop 0
	global_load_lds_dwordx4 v[232:233], off
	v_lshl_add_u64 v[232:233], s[20:21], 0, v[134:135]
	s_mov_b32 m0, s28
	s_nop 0
	global_load_lds_dwordx4 v[232:233], off
	s_mov_b32 m0, s29
	s_nop 0
	global_load_lds_dwordx4 v[234:235], off
	s_waitcnt vmcnt(8)
	s_waitcnt lgkmcnt(0)
	s_barrier
	s_nop 0
	s_waitcnt lgkmcnt(0)
	v_mfma_f32_16x16x32_bf16 v[64:67], v[146:149], v[178:181], v[64:67]
	v_mfma_f32_16x16x32_bf16 v[60:63], v[154:157], v[178:181], v[60:63]
	v_mfma_f32_16x16x32_bf16 v[48:51], v[146:149], v[186:189], v[48:51]
	v_mfma_f32_16x16x32_bf16 v[44:47], v[154:157], v[186:189], v[44:47]
	v_mfma_f32_16x16x32_bf16 v[32:35], v[146:149], v[204:207], v[32:35]
	v_mfma_f32_16x16x32_bf16 v[28:31], v[154:157], v[204:207], v[28:31]
	v_mfma_f32_16x16x32_bf16 v[16:19], v[146:149], v[212:215], v[16:19]
	v_mfma_f32_16x16x32_bf16 v[12:15], v[154:157], v[212:215], v[12:15]
	v_mfma_f32_16x16x32_bf16 v[64:67], v[150:153], v[182:185], v[64:67]
	v_mfma_f32_16x16x32_bf16 v[60:63], v[158:161], v[182:185], v[60:63]
	v_mfma_f32_16x16x32_bf16 v[48:51], v[150:153], v[190:193], v[48:51]
	v_mfma_f32_16x16x32_bf16 v[44:47], v[158:161], v[190:193], v[44:47]
	v_mfma_f32_16x16x32_bf16 v[32:35], v[150:153], v[208:211], v[32:35]
	v_mfma_f32_16x16x32_bf16 v[28:31], v[158:161], v[208:211], v[28:31]
	v_mfma_f32_16x16x32_bf16 v[16:19], v[150:153], v[226:229], v[16:19]
	v_mfma_f32_16x16x32_bf16 v[12:15], v[158:161], v[226:229], v[12:15]
	s_nop 0
	s_nop 0
	v_mfma_f32_16x16x32_bf16 v[56:59], v[162:165], v[178:181], v[56:59]
	v_mfma_f32_16x16x32_bf16 v[52:55], v[170:173], v[178:181], v[52:55]
	v_mfma_f32_16x16x32_bf16 v[40:43], v[162:165], v[186:189], v[40:43]
	v_mfma_f32_16x16x32_bf16 v[36:39], v[170:173], v[186:189], v[36:39]
	v_mfma_f32_16x16x32_bf16 v[24:27], v[162:165], v[204:207], v[24:27]
	v_mfma_f32_16x16x32_bf16 v[20:23], v[170:173], v[204:207], v[20:23]
	v_mfma_f32_16x16x32_bf16 v[8:11], v[162:165], v[212:215], v[8:11]
	v_mfma_f32_16x16x32_bf16 v[4:7], v[170:173], v[212:215], v[4:7]
	v_mfma_f32_16x16x32_bf16 v[56:59], v[166:169], v[182:185], v[56:59]
	v_mfma_f32_16x16x32_bf16 v[52:55], v[174:177], v[182:185], v[52:55]
	v_mfma_f32_16x16x32_bf16 v[40:43], v[166:169], v[190:193], v[40:43]
	v_mfma_f32_16x16x32_bf16 v[36:39], v[174:177], v[190:193], v[36:39]
	v_mfma_f32_16x16x32_bf16 v[24:27], v[166:169], v[208:211], v[24:27]
	v_mfma_f32_16x16x32_bf16 v[20:23], v[174:177], v[208:211], v[20:23]
	v_mfma_f32_16x16x32_bf16 v[8:11], v[166:169], v[226:229], v[8:11]
	v_mfma_f32_16x16x32_bf16 v[4:7], v[174:177], v[226:229], v[4:7]
	s_nop 0
	s_barrier
	s_add_i32 s44, 0, 0x18000
	v_add_u32_e32 v2, s44, v1
	s_add_i32 s45, 0, 0x1c000
	ds_read_b128 v[146:149], v2
	ds_read_b128 v[150:153], v2 offset:1024
	ds_read_b128 v[154:157], v2 offset:2048
	ds_read_b128 v[158:161], v2 offset:3072
	v_add_u32_e32 v2, s45, v1
	ds_read_b128 v[162:165], v2
	ds_read_b128 v[166:169], v2 offset:1024
	ds_read_b128 v[170:173], v2 offset:2048
	ds_read_b128 v[174:177], v2 offset:3072
	s_add_u32 s20, s20, 0x80000
	s_addc_u32 s21, s21, 0
	s_mov_b32 m0, s30
	v_lshl_add_u64 v[236:237], s[20:21], 0, v[134:135]
	ds_read_b128 v[178:181], v144 offset:32768
	ds_read_b128 v[182:185], v144 offset:33792
	ds_read_b128 v[186:189], v144 offset:34816
	ds_read_b128 v[190:193], v144 offset:35840
	ds_read_b128 v[204:207], v144 offset:36864
	ds_read_b128 v[208:211], v144 offset:37888
	ds_read_b128 v[212:215], v144 offset:38912
	ds_read_b128 v[226:229], v144 offset:39936
	global_load_lds_dwordx4 v[236:237], off
	v_lshl_add_u64 v[236:237], s[20:21], 0, v[138:139]
	s_mov_b32 m0, s31
	s_nop 0
	global_load_lds_dwordx4 v[236:237], off
	s_waitcnt vmcnt(8)
	s_waitcnt lgkmcnt(0)
	s_barrier
	s_nop 0
	s_waitcnt lgkmcnt(0)
	v_mfma_f32_16x16x32_bf16 v[128:131], v[146:149], v[178:181], v[128:131]
	v_mfma_f32_16x16x32_bf16 v[124:127], v[154:157], v[178:181], v[124:127]
	v_mfma_f32_16x16x32_bf16 v[112:115], v[146:149], v[186:189], v[112:115]
	v_mfma_f32_16x16x32_bf16 v[108:111], v[154:157], v[186:189], v[108:111]
	v_mfma_f32_16x16x32_bf16 v[96:99], v[146:149], v[204:207], v[96:99]
	v_mfma_f32_16x16x32_bf16 v[92:95], v[154:157], v[204:207], v[92:95]
	v_mfma_f32_16x16x32_bf16 v[80:83], v[146:149], v[212:215], v[80:83]
	v_mfma_f32_16x16x32_bf16 v[76:79], v[154:157], v[212:215], v[76:79]
	v_mfma_f32_16x16x32_bf16 v[128:131], v[150:153], v[182:185], v[128:131]
	v_mfma_f32_16x16x32_bf16 v[124:127], v[158:161], v[182:185], v[124:127]
	v_mfma_f32_16x16x32_bf16 v[112:115], v[150:153], v[190:193], v[112:115]
	v_mfma_f32_16x16x32_bf16 v[108:111], v[158:161], v[190:193], v[108:111]
	v_mfma_f32_16x16x32_bf16 v[96:99], v[150:153], v[208:211], v[96:99]
	v_mfma_f32_16x16x32_bf16 v[92:95], v[158:161], v[208:211], v[92:95]
	v_mfma_f32_16x16x32_bf16 v[80:83], v[150:153], v[226:229], v[80:83]
	v_mfma_f32_16x16x32_bf16 v[76:79], v[158:161], v[226:229], v[76:79]
	s_nop 0
	s_nop 0
	v_mfma_f32_16x16x32_bf16 v[120:123], v[162:165], v[178:181], v[120:123]
	v_mfma_f32_16x16x32_bf16 v[116:119], v[170:173], v[178:181], v[116:119]
	v_mfma_f32_16x16x32_bf16 v[104:107], v[162:165], v[186:189], v[104:107]
	v_mfma_f32_16x16x32_bf16 v[100:103], v[170:173], v[186:189], v[100:103]
	v_mfma_f32_16x16x32_bf16 v[88:91], v[162:165], v[204:207], v[88:91]
	v_mfma_f32_16x16x32_bf16 v[84:87], v[170:173], v[204:207], v[84:87]
	v_mfma_f32_16x16x32_bf16 v[72:75], v[162:165], v[212:215], v[72:75]
	v_mfma_f32_16x16x32_bf16 v[68:71], v[170:173], v[212:215], v[68:71]
	v_mfma_f32_16x16x32_bf16 v[120:123], v[166:169], v[182:185], v[120:123]
	v_mfma_f32_16x16x32_bf16 v[116:119], v[174:177], v[182:185], v[116:119]
	v_mfma_f32_16x16x32_bf16 v[104:107], v[166:169], v[190:193], v[104:107]
	v_mfma_f32_16x16x32_bf16 v[100:103], v[174:177], v[190:193], v[100:103]
	v_mfma_f32_16x16x32_bf16 v[88:91], v[166:169], v[208:211], v[88:91]
	v_mfma_f32_16x16x32_bf16 v[84:87], v[174:177], v[208:211], v[84:87]
	v_mfma_f32_16x16x32_bf16 v[72:75], v[166:169], v[226:229], v[72:75]
	v_mfma_f32_16x16x32_bf16 v[68:71], v[174:177], v[226:229], v[68:71]
	s_nop 0
	s_barrier
	s_add_i32 s20, s44, s27
	v_lshl_add_u64 v[194:195], v[194:195], 0, s[94:95]
	s_mov_b32 m0, s20
	ds_read_b128 v[178:181], v144 offset:49152
	ds_read_b128 v[182:185], v144 offset:50176
	ds_read_b128 v[186:189], v144 offset:51200
	ds_read_b128 v[190:193], v144 offset:52224
	ds_read_b128 v[204:207], v144 offset:53248
	ds_read_b128 v[208:211], v144 offset:54272
	ds_read_b128 v[212:215], v144 offset:55296
	ds_read_b128 v[226:229], v144 offset:56320
	global_load_lds_dwordx4 v[194:195], off
	s_add_i32 m0, s20, 0x2000
	s_add_u32 s18, s18, 0x80080
	v_lshl_add_u64 v[194:195], v[230:231], 0, s[94:95]
	s_addc_u32 s19, s19, 0
	s_add_i32 s20, s45, s27
	global_load_lds_dwordx4 v[194:195], off
	v_lshl_add_u64 v[194:195], s[18:19], 0, v[132:133]
	s_mov_b32 m0, s20
	s_nop 0
	global_load_lds_dwordx4 v[194:195], off
	v_lshl_add_u64 v[194:195], s[18:19], 0, v[136:137]
	s_add_i32 m0, s20, 0x2000
	s_nop 0
	global_load_lds_dwordx4 v[194:195], off
	v_lshl_add_u64 v[194:195], v[232:233], 0, s[94:95]
	s_mov_b32 m0, s36
	s_nop 0
	global_load_lds_dwordx4 v[194:195], off
	v_lshl_add_u64 v[194:195], v[234:235], 0, s[94:95]
	s_mov_b32 m0, s37
	s_nop 0
	global_load_lds_dwordx4 v[194:195], off
	s_waitcnt vmcnt(8)
	s_waitcnt lgkmcnt(0)
	s_barrier
	s_nop 0
	s_waitcnt lgkmcnt(0)
	v_mfma_f32_16x16x32_bf16 v[64:67], v[146:149], v[178:181], v[64:67]
	v_mfma_f32_16x16x32_bf16 v[60:63], v[154:157], v[178:181], v[60:63]
	v_mfma_f32_16x16x32_bf16 v[48:51], v[146:149], v[186:189], v[48:51]
	v_mfma_f32_16x16x32_bf16 v[44:47], v[154:157], v[186:189], v[44:47]
	v_mfma_f32_16x16x32_bf16 v[32:35], v[146:149], v[204:207], v[32:35]
	v_mfma_f32_16x16x32_bf16 v[28:31], v[154:157], v[204:207], v[28:31]
	v_mfma_f32_16x16x32_bf16 v[16:19], v[146:149], v[212:215], v[16:19]
	v_mfma_f32_16x16x32_bf16 v[12:15], v[154:157], v[212:215], v[12:15]
	v_mfma_f32_16x16x32_bf16 v[64:67], v[150:153], v[182:185], v[64:67]
	v_mfma_f32_16x16x32_bf16 v[60:63], v[158:161], v[182:185], v[60:63]
	v_mfma_f32_16x16x32_bf16 v[48:51], v[150:153], v[190:193], v[48:51]
	v_mfma_f32_16x16x32_bf16 v[44:47], v[158:161], v[190:193], v[44:47]
	v_mfma_f32_16x16x32_bf16 v[32:35], v[150:153], v[208:211], v[32:35]
	v_mfma_f32_16x16x32_bf16 v[28:31], v[158:161], v[208:211], v[28:31]
	v_mfma_f32_16x16x32_bf16 v[16:19], v[150:153], v[226:229], v[16:19]
	v_mfma_f32_16x16x32_bf16 v[12:15], v[158:161], v[226:229], v[12:15]
	s_nop 0
	s_nop 0
	v_mfma_f32_16x16x32_bf16 v[56:59], v[162:165], v[178:181], v[56:59]
	v_mfma_f32_16x16x32_bf16 v[52:55], v[170:173], v[178:181], v[52:55]
	v_mfma_f32_16x16x32_bf16 v[40:43], v[162:165], v[186:189], v[40:43]
	v_mfma_f32_16x16x32_bf16 v[36:39], v[170:173], v[186:189], v[36:39]
	v_mfma_f32_16x16x32_bf16 v[24:27], v[162:165], v[204:207], v[24:27]
	v_mfma_f32_16x16x32_bf16 v[20:23], v[170:173], v[204:207], v[20:23]
	v_mfma_f32_16x16x32_bf16 v[8:11], v[162:165], v[212:215], v[8:11]
	v_mfma_f32_16x16x32_bf16 v[4:7], v[170:173], v[212:215], v[4:7]
	v_mfma_f32_16x16x32_bf16 v[56:59], v[166:169], v[182:185], v[56:59]
	v_mfma_f32_16x16x32_bf16 v[52:55], v[174:177], v[182:185], v[52:55]
	v_mfma_f32_16x16x32_bf16 v[40:43], v[166:169], v[190:193], v[40:43]
	v_mfma_f32_16x16x32_bf16 v[36:39], v[174:177], v[190:193], v[36:39]
	v_mfma_f32_16x16x32_bf16 v[24:27], v[166:169], v[208:211], v[24:27]
	v_mfma_f32_16x16x32_bf16 v[20:23], v[174:177], v[208:211], v[20:23]
	v_mfma_f32_16x16x32_bf16 v[8:11], v[166:169], v[226:229], v[8:11]
	v_mfma_f32_16x16x32_bf16 v[4:7], v[174:177], v[226:229], v[4:7]
	s_nop 0
	s_barrier
	s_add_i32 s43, s43, 2
	s_add_u32 s7, s7, 0x100
	s_addc_u32 s42, s42, 0
	s_add_u32 s16, s16, 0x100
	s_addc_u32 s17, s17, 0
	s_cmp_gt_u32 s43, 29
	s_cbranch_scc0 .LBB0_724
	s_and_b64 vcc, exec, s[10:11]
	s_cbranch_vccz .LBB0_727
	s_barrier

.LBB0_747:
	s_add_i32 s18, s91, 3
	s_cmp_ge_i32 s18, s67
	s_cbranch_scc1 .LBB0_758
	s_waitcnt vmcnt(0)
	s_waitcnt vmcnt(0) lgkmcnt(0)
	s_barrier
	s_setprio 0
	s_mov_b64 s[2:3], exec
	v_readlane_b32 s4, v243, 59
	v_readlane_b32 s5, v243, 60
	v_readlane_b32 s92, v242, 25
	s_and_b64 s[4:5], s[2:3], s[4:5]
	v_readlane_b32 s93, v242, 26
	s_movk_i32 s89, 0x2000
	s_mov_b32 s90, 0x40e00000
	s_mov_b64 exec, s[4:5]
	s_cbranch_execz .LBB0_796
	v_readlane_b32 s4, v243, 56
	s_waitcnt vmcnt(0) expcnt(0) lgkmcnt(0)
	s_nop 0
	v_mov_b32_e32 v1, s4
	ds_read_b32 v4, v1
	ds_read_b32 v2, v1 offset:4
	s_waitcnt lgkmcnt(1)
	v_cmp_ne_u32_e32 vcc, 0, v4
	s_cbranch_vccnz .LBB0_764
	s_load_dwordx2 s[4:5], s[0:1], 0x0
	s_load_dword s6, s[0:1], 0x8
	s_mov_b32 s10, 0
	s_waitcnt lgkmcnt(0)
	s_mul_i32 s9, s5, s4
	s_mul_i32 s9, s9, s6
	s_branch .LBB0_752

.LBB0_840:
	s_add_i32 s18, s91, 4
	s_cmp_lt_i32 s18, s67
	s_cbranch_scc0 .LBB0_889
	s_waitcnt vmcnt(0)
	s_barrier
	s_setprio 0
	s_mov_b64 s[2:3], exec
	v_readlane_b32 s4, v243, 59
	v_readlane_b32 s5, v243, 60
	s_and_b64 s[4:5], s[2:3], s[4:5]
	s_mov_b64 exec, s[4:5]
	s_cbranch_execz .LBB0_888
	v_readlane_b32 s4, v243, 56
	s_waitcnt vmcnt(0) expcnt(0) lgkmcnt(0)
	s_nop 0
	v_mov_b32_e32 v1, s4
	ds_read_b32 v4, v1
	ds_read_b32 v2, v1 offset:4
	s_waitcnt lgkmcnt(1)
	v_cmp_ne_u32_e32 vcc, 0, v4
	s_cbranch_vccnz .LBB0_856
	s_load_dwordx2 s[4:5], s[0:1], 0x0
	s_load_dword s6, s[0:1], 0x8
	s_mov_b32 s10, 0
	s_waitcnt lgkmcnt(0)
	s_mul_i32 s9, s5, s4
	s_mul_i32 s9, s9, s6
	s_branch .LBB0_845

.LBB0_896:
	s_andn2_b64 vcc, exec, s[6:7]
	s_cbranch_vccnz .LBB0_980
	s_waitcnt vmcnt(0)
	v_bfe_i32 v5, v1, 27, 1
	v_lshlrev_b32_e32 v4, 4, v1
	v_lshrrev_b32_e32 v5, 22, v5
	v_add_u32_e32 v5, v4, v5
	v_and_b32_e32 v5, 0xfffffc00, v5
	v_sub_u32_e32 v5, v4, v5
	v_lshrrev_b32_e32 v6, 4, v5
	v_ashrrev_i32_e32 v2, 31, v1
	v_bitop3_b32 v5, v6, v5, 32 bitop3:0x6c
	v_lshrrev_b32_e32 v2, 26, v2
	v_ashrrev_i32_e32 v7, 31, v5
	v_add_u32_e32 v2, v1, v2
	v_lshrrev_b32_e32 v7, 26, v7
	v_ashrrev_i32_e32 v2, 6, v2
	v_add_u32_e32 v7, v5, v7
	v_lshlrev_b32_e32 v6, 3, v2
	v_ashrrev_i32_e32 v12, 6, v7
	v_and_b32_e32 v7, 0xc0, v7
	v_and_b32_e32 v6, -16, v6
	v_sub_u32_e32 v5, v5, v7
	v_add_u32_e32 v6, v12, v6
	v_ashrrev_i16_sdwa v5, v216, sext(v5) dst_sel:DWORD dst_unused:UNUSED_PAD src0_sel:DWORD src1_sel:BYTE_0
	v_lshlrev_b32_e32 v8, 5, v2
	v_bfe_i32 v13, v5, 0, 16
	v_lshlrev_b32_e32 v5, 1, v6
	v_lshrrev_b32_e32 v7, 2, v6
	v_and_b32_e32 v9, 3, v12
	s_mov_b32 s6, 0xfffe0
	v_and_b32_e32 v8, 32, v8
	v_and_b32_e32 v5, 24, v5
	v_and_b32_e32 v7, 4, v7
	v_and_or_b32 v9, v6, s6, v9
	v_or3_b32 v5, v9, v7, v5
	v_add_lshl_u32 v7, v8, v13, 1
	v_add_u32_e32 v4, 0x2000, v4
	v_lshl_add_u32 v140, v5, 12, v7
	v_ashrrev_i32_e32 v5, 31, v4
	v_lshrrev_b32_e32 v5, 22, v5
	v_add_u32_e32 v5, v4, v5
	v_ashrrev_i32_e32 v14, 10, v5
	v_mul_i32_i24_e32 v5, 0x400, v14
	v_sub_u32_e32 v4, v4, v5
	v_lshrrev_b32_e32 v5, 4, v4
	v_bitop3_b32 v4, v5, v4, 32 bitop3:0x6c
	v_lshl_add_u32 v142, v6, 12, v7
	v_ashrrev_i32_e32 v6, 31, v4
	v_lshrrev_b32_e32 v6, 26, v6
	v_add_u32_e32 v6, v4, v6
	v_lshlrev_b32_e32 v5, 3, v14
	v_ashrrev_i32_e32 v15, 6, v6
	v_and_b32_e32 v6, 0xc0, v6
	s_ashr_i32 s15, s14, 6
	v_and_b32_e32 v5, -16, v5
	v_sub_u32_e32 v4, v4, v6
	v_add_u32_e32 v5, v15, v5
	v_ashrrev_i16_sdwa v4, v216, sext(v4) dst_sel:DWORD dst_unused:UNUSED_PAD src0_sel:DWORD src1_sel:BYTE_0
	s_lshl_b32 s34, s15, 10
	v_lshlrev_b32_e32 v7, 5, v14
	v_bfe_i32 v16, v4, 0, 16
	v_lshlrev_b32_e32 v4, 1, v5
	v_lshrrev_b32_e32 v6, 2, v5
	v_and_b32_e32 v8, 3, v15
	s_add_i32 s35, s34, 0
	v_and_b32_e32 v7, 32, v7
	v_and_b32_e32 v4, 24, v4
	v_and_b32_e32 v6, 4, v6
	v_and_or_b32 v8, v5, s6, v8
	s_waitcnt lgkmcnt(0)
	s_add_i32 m0, s35, 0x10000
	v_or3_b32 v4, v8, v6, v4
	v_add_lshl_u32 v6, v7, v16, 1
	s_ashr_i32 s16, s14, 8
	global_load_lds_dwordx4 v140, s[22:23]
	s_add_i32 m0, s35, 0x12000
	v_lshl_add_u32 v144, v4, 12, v6
	s_add_u32 s6, s22, 0x80000
	global_load_lds_dwordx4 v144, s[22:23]
	s_addc_u32 s7, s23, 0
	s_add_i32 m0, s35, 0x14000
	s_add_i32 s36, s35, 0x2000
	global_load_lds_dwordx4 v140, s[6:7]
	s_add_i32 m0, s35, 0x16000
	v_lshl_add_u32 v146, v5, 12, v6
	global_load_lds_dwordx4 v144, s[6:7]
	s_mov_b32 m0, s35
	s_add_u32 s6, s4, 0x80000
	global_load_lds_dwordx4 v142, s[4:5]
	s_mov_b32 m0, s36
	s_addc_u32 s7, s5, 0
	s_add_i32 s37, s35, 0x4000
	global_load_lds_dwordx4 v146, s[4:5]
	s_mov_b32 m0, s37
	s_add_i32 s38, s35, 0x6000
	global_load_lds_dwordx4 v142, s[6:7]
	s_mov_b32 m0, s38
	s_mov_b64 s[74:75], s[66:67]
	global_load_lds_dwordx4 v146, s[6:7]
	v_mov_b32_e32 v141, v3
	v_mov_b32_e32 v145, v3
	v_mov_b32_e32 v143, v3
	v_mov_b32_e32 v147, v3
	s_cmp_eq_u32 s16, 1
	s_mov_b64 s[72:73], s[64:65]
	s_mov_b64 s[70:71], s[62:63]
	v_lshl_add_u64 v[10:11], s[22:23], 0, v[140:141]
	v_lshl_add_u64 v[8:9], s[22:23], 0, v[144:145]
	v_lshl_add_u64 v[4:5], s[4:5], 0, v[142:143]
	s_cselect_b64 s[6:7], -1, 0
	s_cmp_lg_u32 s16, 1
	v_lshl_add_u64 v[6:7], s[4:5], 0, v[146:147]
	s_cbranch_scc1 .LBB0_899
	s_barrier
	s_setprio 1

.LBB0_909:
	s_add_u32 s22, s4, 0xfff80080
	s_addc_u32 s23, s5, -1
	s_add_i32 s55, 0, 0x10000
	s_cmp_eq_u32 s54, 28
	s_cselect_b32 s25, s19, s23
	s_cselect_b32 s24, s18, s22
	v_add_u32_e32 v2, s55, v1
	s_cselect_b32 s23, s21, s53
	s_cselect_b32 s22, s20, s52
	s_add_i32 s58, 0, 0x14000
	ds_read_b128 v[132:135], v2
	ds_read_b128 v[136:139], v2 offset:1024
	ds_read_b128 v[152:155], v2 offset:2048
	ds_read_b128 v[156:159], v2 offset:3072
	v_add_u32_e32 v2, s58, v1
	ds_read_b128 v[164:167], v2
	ds_read_b128 v[168:171], v2 offset:1024
	ds_read_b128 v[172:175], v2 offset:2048
	ds_read_b128 v[176:179], v2 offset:3072
	v_lshl_add_u64 v[160:161], s[4:5], 0, v[150:151]
	s_add_i32 m0, s35, 0xc000
	ds_read_b128 v[180:183], v162
	ds_read_b128 v[184:187], v162 offset:1024
	ds_read_b128 v[188:191], v162 offset:2048
	ds_read_b128 v[192:195], v162 offset:3072
	ds_read_b128 v[204:207], v162 offset:4096
	ds_read_b128 v[208:211], v162 offset:5120
	ds_read_b128 v[212:215], v162 offset:6144
	ds_read_b128 v[226:229], v162 offset:7168
	global_load_lds_dwordx4 v[160:161], off
	v_lshl_add_u64 v[160:161], s[4:5], 0, v[148:149]
	s_add_i32 m0, s35, 0xe000
	s_nop 0
	global_load_lds_dwordx4 v[160:161], off
	s_waitcnt vmcnt(8)
	s_waitcnt lgkmcnt(0)
	s_barrier
	s_nop 0
	s_waitcnt lgkmcnt(0)
	v_mfma_f32_16x16x32_bf16 v[128:131], v[132:135], v[180:183], v[128:131]
	v_mfma_f32_16x16x32_bf16 v[124:127], v[152:155], v[180:183], v[124:127]
	v_mfma_f32_16x16x32_bf16 v[112:115], v[132:135], v[188:191], v[112:115]
	v_mfma_f32_16x16x32_bf16 v[108:111], v[152:155], v[188:191], v[108:111]
	v_mfma_f32_16x16x32_bf16 v[96:99], v[132:135], v[204:207], v[96:99]
	v_mfma_f32_16x16x32_bf16 v[92:95], v[152:155], v[204:207], v[92:95]
	v_mfma_f32_16x16x32_bf16 v[80:83], v[132:135], v[212:215], v[80:83]
	v_mfma_f32_16x16x32_bf16 v[76:79], v[152:155], v[212:215], v[76:79]
	v_mfma_f32_16x16x32_bf16 v[128:131], v[136:139], v[184:187], v[128:131]
	v_mfma_f32_16x16x32_bf16 v[124:127], v[156:159], v[184:187], v[124:127]
	v_mfma_f32_16x16x32_bf16 v[112:115], v[136:139], v[192:195], v[112:115]
	v_mfma_f32_16x16x32_bf16 v[108:111], v[156:159], v[192:195], v[108:111]
	v_mfma_f32_16x16x32_bf16 v[96:99], v[136:139], v[208:211], v[96:99]
	v_mfma_f32_16x16x32_bf16 v[92:95], v[156:159], v[208:211], v[92:95]
	v_mfma_f32_16x16x32_bf16 v[80:83], v[136:139], v[226:229], v[80:83]
	v_mfma_f32_16x16x32_bf16 v[76:79], v[156:159], v[226:229], v[76:79]
	s_nop 0
	s_nop 0
	v_mfma_f32_16x16x32_bf16 v[120:123], v[164:167], v[180:183], v[120:123]
	v_mfma_f32_16x16x32_bf16 v[116:119], v[172:175], v[180:183], v[116:119]
	v_mfma_f32_16x16x32_bf16 v[104:107], v[164:167], v[188:191], v[104:107]
	v_mfma_f32_16x16x32_bf16 v[100:103], v[172:175], v[188:191], v[100:103]
	v_mfma_f32_16x16x32_bf16 v[88:91], v[164:167], v[204:207], v[88:91]
	v_mfma_f32_16x16x32_bf16 v[84:87], v[172:175], v[204:207], v[84:87]
	v_mfma_f32_16x16x32_bf16 v[72:75], v[164:167], v[212:215], v[72:75]
	v_mfma_f32_16x16x32_bf16 v[68:71], v[172:175], v[212:215], v[68:71]
	v_mfma_f32_16x16x32_bf16 v[120:123], v[168:171], v[184:187], v[120:123]
	v_mfma_f32_16x16x32_bf16 v[116:119], v[176:179], v[184:187], v[116:119]
	v_mfma_f32_16x16x32_bf16 v[104:107], v[168:171], v[192:195], v[104:107]
	v_mfma_f32_16x16x32_bf16 v[100:103], v[176:179], v[192:195], v[100:103]
	v_mfma_f32_16x16x32_bf16 v[88:91], v[168:171], v[208:211], v[88:91]
	v_mfma_f32_16x16x32_bf16 v[84:87], v[176:179], v[208:211], v[84:87]
	v_mfma_f32_16x16x32_bf16 v[72:75], v[168:171], v[226:229], v[72:75]
	v_mfma_f32_16x16x32_bf16 v[68:71], v[176:179], v[226:229], v[68:71]
	s_nop 0
	s_barrier
	s_add_i32 s55, s55, s34
	v_lshl_add_u64 v[160:161], s[22:23], 0, v[140:141]
	s_mov_b32 m0, s55
	ds_read_b128 v[180:183], v162 offset:16384
	ds_read_b128 v[184:187], v162 offset:17408
	ds_read_b128 v[188:191], v162 offset:18432
	ds_read_b128 v[192:195], v162 offset:19456
	ds_read_b128 v[204:207], v162 offset:20480
	ds_read_b128 v[208:211], v162 offset:21504
	ds_read_b128 v[212:215], v162 offset:22528
	ds_read_b128 v[226:229], v162 offset:23552
	global_load_lds_dwordx4 v[160:161], off
	s_add_i32 m0, s55, 0x2000
	s_add_u32 s56, s22, 0x80000
	v_lshl_add_u64 v[230:231], s[22:23], 0, v[144:145]
	s_addc_u32 s57, s23, 0
	s_add_i32 s55, s58, s34
	global_load_lds_dwordx4 v[230:231], off
	v_lshl_add_u64 v[232:233], s[56:57], 0, v[140:141]
	s_mov_b32 m0, s55
	v_lshl_add_u64 v[234:235], s[24:25], 0, v[146:147]
	global_load_lds_dwordx4 v[232:233], off
	v_lshl_add_u64 v[232:233], s[56:57], 0, v[144:145]
	s_add_i32 m0, s55, 0x2000
	s_nop 0
	global_load_lds_dwordx4 v[232:233], off
	v_lshl_add_u64 v[232:233], s[24:25], 0, v[142:143]
	s_mov_b32 m0, s35
	s_nop 0
	global_load_lds_dwordx4 v[232:233], off
	s_mov_b32 m0, s36
	s_nop 0
	global_load_lds_dwordx4 v[234:235], off
	s_waitcnt vmcnt(8)
	s_waitcnt lgkmcnt(0)
	s_barrier
	s_nop 0
	s_waitcnt lgkmcnt(0)
	v_mfma_f32_16x16x32_bf16 v[64:67], v[132:135], v[180:183], v[64:67]
	v_mfma_f32_16x16x32_bf16 v[60:63], v[152:155], v[180:183], v[60:63]
	v_mfma_f32_16x16x32_bf16 v[48:51], v[132:135], v[188:191], v[48:51]
	v_mfma_f32_16x16x32_bf16 v[44:47], v[152:155], v[188:191], v[44:47]
	v_mfma_f32_16x16x32_bf16 v[32:35], v[132:135], v[204:207], v[32:35]
	v_mfma_f32_16x16x32_bf16 v[28:31], v[152:155], v[204:207], v[28:31]
	v_mfma_f32_16x16x32_bf16 v[16:19], v[132:135], v[212:215], v[16:19]
	v_mfma_f32_16x16x32_bf16 v[12:15], v[152:155], v[212:215], v[12:15]
	v_mfma_f32_16x16x32_bf16 v[64:67], v[136:139], v[184:187], v[64:67]
	v_mfma_f32_16x16x32_bf16 v[60:63], v[156:159], v[184:187], v[60:63]
	v_mfma_f32_16x16x32_bf16 v[48:51], v[136:139], v[192:195], v[48:51]
	v_mfma_f32_16x16x32_bf16 v[44:47], v[156:159], v[192:195], v[44:47]
	v_mfma_f32_16x16x32_bf16 v[32:35], v[136:139], v[208:211], v[32:35]
	v_mfma_f32_16x16x32_bf16 v[28:31], v[156:159], v[208:211], v[28:31]
	v_mfma_f32_16x16x32_bf16 v[16:19], v[136:139], v[226:229], v[16:19]
	v_mfma_f32_16x16x32_bf16 v[12:15], v[156:159], v[226:229], v[12:15]
	s_nop 0
	s_nop 0
	v_mfma_f32_16x16x32_bf16 v[56:59], v[164:167], v[180:183], v[56:59]
	v_mfma_f32_16x16x32_bf16 v[52:55], v[172:175], v[180:183], v[52:55]
	v_mfma_f32_16x16x32_bf16 v[40:43], v[164:167], v[188:191], v[40:43]
	v_mfma_f32_16x16x32_bf16 v[36:39], v[172:175], v[188:191], v[36:39]
	v_mfma_f32_16x16x32_bf16 v[24:27], v[164:167], v[204:207], v[24:27]
	v_mfma_f32_16x16x32_bf16 v[20:23], v[172:175], v[204:207], v[20:23]
	v_mfma_f32_16x16x32_bf16 v[8:11], v[164:167], v[212:215], v[8:11]
	v_mfma_f32_16x16x32_bf16 v[4:7], v[172:175], v[212:215], v[4:7]
	v_mfma_f32_16x16x32_bf16 v[56:59], v[168:171], v[184:187], v[56:59]
	v_mfma_f32_16x16x32_bf16 v[52:55], v[176:179], v[184:187], v[52:55]
	v_mfma_f32_16x16x32_bf16 v[40:43], v[168:171], v[192:195], v[40:43]
	v_mfma_f32_16x16x32_bf16 v[36:39], v[176:179], v[192:195], v[36:39]
	v_mfma_f32_16x16x32_bf16 v[24:27], v[168:171], v[208:211], v[24:27]
	v_mfma_f32_16x16x32_bf16 v[20:23], v[176:179], v[208:211], v[20:23]
	v_mfma_f32_16x16x32_bf16 v[8:11], v[168:171], v[226:229], v[8:11]
	v_mfma_f32_16x16x32_bf16 v[4:7], v[176:179], v[226:229], v[4:7]
	s_nop 0
	s_barrier
	s_add_i32 s55, 0, 0x18000
	v_add_u32_e32 v2, s55, v1
	s_add_i32 s56, 0, 0x1c000
	ds_read_b128 v[132:135], v2
	ds_read_b128 v[136:139], v2 offset:1024
	ds_read_b128 v[152:155], v2 offset:2048
	ds_read_b128 v[156:159], v2 offset:3072
	v_add_u32_e32 v2, s56, v1
	ds_read_b128 v[164:167], v2
	ds_read_b128 v[168:171], v2 offset:1024
	ds_read_b128 v[172:175], v2 offset:2048
	ds_read_b128 v[176:179], v2 offset:3072
	s_add_u32 s24, s24, 0x80000
	s_addc_u32 s25, s25, 0
	s_mov_b32 m0, s37
	v_lshl_add_u64 v[236:237], s[24:25], 0, v[142:143]
	ds_read_b128 v[180:183], v162 offset:32768
	ds_read_b128 v[184:187], v162 offset:33792
	ds_read_b128 v[188:191], v162 offset:34816
	ds_read_b128 v[192:195], v162 offset:35840
	ds_read_b128 v[204:207], v162 offset:36864
	ds_read_b128 v[208:211], v162 offset:37888
	ds_read_b128 v[212:215], v162 offset:38912
	ds_read_b128 v[226:229], v162 offset:39936
	global_load_lds_dwordx4 v[236:237], off
	v_lshl_add_u64 v[236:237], s[24:25], 0, v[146:147]
	s_mov_b32 m0, s38
	s_nop 0
	global_load_lds_dwordx4 v[236:237], off
	s_waitcnt vmcnt(8)
	s_waitcnt lgkmcnt(0)
	s_barrier
	s_nop 0
	s_waitcnt lgkmcnt(0)
	v_mfma_f32_16x16x32_bf16 v[128:131], v[132:135], v[180:183], v[128:131]
	v_mfma_f32_16x16x32_bf16 v[124:127], v[152:155], v[180:183], v[124:127]
	v_mfma_f32_16x16x32_bf16 v[112:115], v[132:135], v[188:191], v[112:115]
	v_mfma_f32_16x16x32_bf16 v[108:111], v[152:155], v[188:191], v[108:111]
	v_mfma_f32_16x16x32_bf16 v[96:99], v[132:135], v[204:207], v[96:99]
	v_mfma_f32_16x16x32_bf16 v[92:95], v[152:155], v[204:207], v[92:95]
	v_mfma_f32_16x16x32_bf16 v[80:83], v[132:135], v[212:215], v[80:83]
	v_mfma_f32_16x16x32_bf16 v[76:79], v[152:155], v[212:215], v[76:79]
	v_mfma_f32_16x16x32_bf16 v[128:131], v[136:139], v[184:187], v[128:131]
	v_mfma_f32_16x16x32_bf16 v[124:127], v[156:159], v[184:187], v[124:127]
	v_mfma_f32_16x16x32_bf16 v[112:115], v[136:139], v[192:195], v[112:115]
	v_mfma_f32_16x16x32_bf16 v[108:111], v[156:159], v[192:195], v[108:111]
	v_mfma_f32_16x16x32_bf16 v[96:99], v[136:139], v[208:211], v[96:99]
	v_mfma_f32_16x16x32_bf16 v[92:95], v[156:159], v[208:211], v[92:95]
	v_mfma_f32_16x16x32_bf16 v[80:83], v[136:139], v[226:229], v[80:83]
	v_mfma_f32_16x16x32_bf16 v[76:79], v[156:159], v[226:229], v[76:79]
	s_nop 0
	s_nop 0
	v_mfma_f32_16x16x32_bf16 v[120:123], v[164:167], v[180:183], v[120:123]
	v_mfma_f32_16x16x32_bf16 v[116:119], v[172:175], v[180:183], v[116:119]
	v_mfma_f32_16x16x32_bf16 v[104:107], v[164:167], v[188:191], v[104:107]
	v_mfma_f32_16x16x32_bf16 v[100:103], v[172:175], v[188:191], v[100:103]
	v_mfma_f32_16x16x32_bf16 v[88:91], v[164:167], v[204:207], v[88:91]
	v_mfma_f32_16x16x32_bf16 v[84:87], v[172:175], v[204:207], v[84:87]
	v_mfma_f32_16x16x32_bf16 v[72:75], v[164:167], v[212:215], v[72:75]
	v_mfma_f32_16x16x32_bf16 v[68:71], v[172:175], v[212:215], v[68:71]
	v_mfma_f32_16x16x32_bf16 v[120:123], v[168:171], v[184:187], v[120:123]
	v_mfma_f32_16x16x32_bf16 v[116:119], v[176:179], v[184:187], v[116:119]
	v_mfma_f32_16x16x32_bf16 v[104:107], v[168:171], v[192:195], v[104:107]
	v_mfma_f32_16x16x32_bf16 v[100:103], v[176:179], v[192:195], v[100:103]
	v_mfma_f32_16x16x32_bf16 v[88:91], v[168:171], v[208:211], v[88:91]
	v_mfma_f32_16x16x32_bf16 v[84:87], v[176:179], v[208:211], v[84:87]
	v_mfma_f32_16x16x32_bf16 v[72:75], v[168:171], v[226:229], v[72:75]
	v_mfma_f32_16x16x32_bf16 v[68:71], v[176:179], v[226:229], v[68:71]
	s_nop 0
	s_barrier
	s_add_i32 s24, s55, s34
	v_lshl_add_u64 v[160:161], v[160:161], 0, s[94:95]
	s_mov_b32 m0, s24
	ds_read_b128 v[180:183], v162 offset:49152
	ds_read_b128 v[184:187], v162 offset:50176
	ds_read_b128 v[188:191], v162 offset:51200
	ds_read_b128 v[192:195], v162 offset:52224
	ds_read_b128 v[204:207], v162 offset:53248
	ds_read_b128 v[208:211], v162 offset:54272
	ds_read_b128 v[212:215], v162 offset:55296
	ds_read_b128 v[226:229], v162 offset:56320
	global_load_lds_dwordx4 v[160:161], off
	s_add_i32 m0, s24, 0x2000
	s_add_u32 s22, s22, 0x80080
	v_lshl_add_u64 v[160:161], v[230:231], 0, s[94:95]
	s_addc_u32 s23, s23, 0
	s_add_i32 s24, s56, s34
	global_load_lds_dwordx4 v[160:161], off
	v_lshl_add_u64 v[160:161], s[22:23], 0, v[140:141]
	s_mov_b32 m0, s24
	s_nop 0
	global_load_lds_dwordx4 v[160:161], off
	v_lshl_add_u64 v[160:161], s[22:23], 0, v[144:145]
	s_add_i32 m0, s24, 0x2000
	s_nop 0
	global_load_lds_dwordx4 v[160:161], off
	v_lshl_add_u64 v[160:161], v[232:233], 0, s[94:95]
	s_mov_b32 m0, s42
	s_nop 0
	global_load_lds_dwordx4 v[160:161], off
	v_lshl_add_u64 v[160:161], v[234:235], 0, s[94:95]
	s_mov_b32 m0, s43
	s_nop 0
	global_load_lds_dwordx4 v[160:161], off
	s_waitcnt vmcnt(8)
	s_waitcnt lgkmcnt(0)
	s_barrier
	s_nop 0
	s_waitcnt lgkmcnt(0)
	v_mfma_f32_16x16x32_bf16 v[64:67], v[132:135], v[180:183], v[64:67]
	v_mfma_f32_16x16x32_bf16 v[60:63], v[152:155], v[180:183], v[60:63]
	v_mfma_f32_16x16x32_bf16 v[48:51], v[132:135], v[188:191], v[48:51]
	v_mfma_f32_16x16x32_bf16 v[44:47], v[152:155], v[188:191], v[44:47]
	v_mfma_f32_16x16x32_bf16 v[32:35], v[132:135], v[204:207], v[32:35]
	v_mfma_f32_16x16x32_bf16 v[28:31], v[152:155], v[204:207], v[28:31]
	v_mfma_f32_16x16x32_bf16 v[16:19], v[132:135], v[212:215], v[16:19]
	v_mfma_f32_16x16x32_bf16 v[12:15], v[152:155], v[212:215], v[12:15]
	v_mfma_f32_16x16x32_bf16 v[64:67], v[136:139], v[184:187], v[64:67]
	v_mfma_f32_16x16x32_bf16 v[60:63], v[156:159], v[184:187], v[60:63]
	v_mfma_f32_16x16x32_bf16 v[48:51], v[136:139], v[192:195], v[48:51]
	v_mfma_f32_16x16x32_bf16 v[44:47], v[156:159], v[192:195], v[44:47]
	v_mfma_f32_16x16x32_bf16 v[32:35], v[136:139], v[208:211], v[32:35]
	v_mfma_f32_16x16x32_bf16 v[28:31], v[156:159], v[208:211], v[28:31]
	v_mfma_f32_16x16x32_bf16 v[16:19], v[136:139], v[226:229], v[16:19]
	v_mfma_f32_16x16x32_bf16 v[12:15], v[156:159], v[226:229], v[12:15]
	s_nop 0
	s_nop 0
	v_mfma_f32_16x16x32_bf16 v[56:59], v[164:167], v[180:183], v[56:59]
	v_mfma_f32_16x16x32_bf16 v[52:55], v[172:175], v[180:183], v[52:55]
	v_mfma_f32_16x16x32_bf16 v[40:43], v[164:167], v[188:191], v[40:43]
	v_mfma_f32_16x16x32_bf16 v[36:39], v[172:175], v[188:191], v[36:39]
	v_mfma_f32_16x16x32_bf16 v[24:27], v[164:167], v[204:207], v[24:27]
	v_mfma_f32_16x16x32_bf16 v[20:23], v[172:175], v[204:207], v[20:23]
	v_mfma_f32_16x16x32_bf16 v[8:11], v[164:167], v[212:215], v[8:11]
	v_mfma_f32_16x16x32_bf16 v[4:7], v[172:175], v[212:215], v[4:7]
	v_mfma_f32_16x16x32_bf16 v[56:59], v[168:171], v[184:187], v[56:59]
	v_mfma_f32_16x16x32_bf16 v[52:55], v[176:179], v[184:187], v[52:55]
	v_mfma_f32_16x16x32_bf16 v[40:43], v[168:171], v[192:195], v[40:43]
	v_mfma_f32_16x16x32_bf16 v[36:39], v[176:179], v[192:195], v[36:39]
	v_mfma_f32_16x16x32_bf16 v[24:27], v[168:171], v[208:211], v[24:27]
	v_mfma_f32_16x16x32_bf16 v[20:23], v[176:179], v[208:211], v[20:23]
	v_mfma_f32_16x16x32_bf16 v[8:11], v[168:171], v[226:229], v[8:11]
	v_mfma_f32_16x16x32_bf16 v[4:7], v[176:179], v[226:229], v[4:7]
	s_nop 0
	s_barrier
	s_add_i32 s54, s54, 2
	s_add_u32 s52, s52, 0x100
	s_addc_u32 s53, s53, 0
	s_add_u32 s4, s4, 0x100
	s_addc_u32 s5, s5, 0
	s_cmp_gt_u32 s54, 29
	s_cbranch_scc0 .LBB0_909
	s_and_b64 vcc, exec, s[14:15]
	s_cbranch_vccz .LBB0_912
	s_barrier

.LBB0_980:
	s_add_i32 s18, s91, 5
	s_cmp_ge_i32 s18, s67
	s_waitcnt vmcnt(0) lgkmcnt(0)
	s_barrier
	s_cbranch_scc1 .LBB0_1029
	s_waitcnt vmcnt(0)
	s_barrier
	s_setprio 0
	s_mov_b64 s[2:3], exec
	v_readlane_b32 s4, v243, 59
	v_readlane_b32 s5, v243, 60
	s_and_b64 s[4:5], s[2:3], s[4:5]
	s_mov_b64 exec, s[4:5]
	s_cbranch_execz .LBB0_1028
	v_readlane_b32 s4, v243, 56
	s_waitcnt vmcnt(0) expcnt(0) lgkmcnt(0)
	s_nop 0
	v_mov_b32_e32 v1, s4
	ds_read_b32 v4, v1
	ds_read_b32 v2, v1 offset:4
	s_waitcnt lgkmcnt(1)
	v_cmp_ne_u32_e32 vcc, 0, v4
	s_cbranch_vccnz .LBB0_996
	s_load_dwordx2 s[4:5], s[0:1], 0x0
	s_load_dword s6, s[0:1], 0x8
	s_mov_b32 s10, 0
	s_waitcnt lgkmcnt(0)
	s_mul_i32 s9, s5, s4
	s_mul_i32 s9, s9, s6
	s_branch .LBB0_985

.LBB0_1570:
	s_add_i32 s2, s76, 0xc300
	s_max_i32 s50, s50, s2
	s_add_i32 s18, s91, 6
	s_cmp_ge_i32 s18, s67
	s_cbranch_scc1 .LBB0_1581
	s_waitcnt vmcnt(0)
	s_waitcnt vmcnt(0) lgkmcnt(0)
	s_barrier
	s_setprio 0
	s_mov_b64 s[2:3], exec
	v_readlane_b32 s4, v243, 59
	v_readlane_b32 s5, v243, 60
	v_readlane_b32 s92, v242, 25
	s_and_b64 s[4:5], s[2:3], s[4:5]
	v_readlane_b32 s93, v242, 26
	s_mov_b64 exec, s[4:5]
	s_cbranch_execz .LBB0_1622
	v_readlane_b32 s4, v243, 56
	s_waitcnt vmcnt(0) expcnt(0) lgkmcnt(0)
	s_nop 0
	v_mov_b32_e32 v1, s4
	ds_read_b32 v4, v1
	ds_read_b32 v2, v1 offset:4
	s_waitcnt lgkmcnt(1)
	v_cmp_ne_u32_e32 vcc, 0, v4
	s_cbranch_vccnz .LBB0_1587
	s_load_dwordx2 s[4:5], s[0:1], 0x4
	s_mov_b32 s10, 0
	s_waitcnt lgkmcnt(0)
	s_mul_i32 s9, s4, s85
	s_mul_i32 s9, s9, s5
	s_branch .LBB0_1575

.LBB0_2105:
	s_andn2_b64 vcc, exec, s[8:9]
	s_cbranch_vccnz .LBB0_2141
	s_waitcnt vmcnt(6)
	v_bfe_i32 v5, v1, 27, 1
	v_lshlrev_b32_e32 v2, 4, v1
	v_lshrrev_b32_e32 v5, 22, v5
	v_add_u32_e32 v5, v2, v5
	v_and_b32_e32 v5, 0xfffffc00, v5
	v_sub_u32_e32 v5, v2, v5
	v_ashrrev_i32_e32 v4, 31, v1
	v_lshrrev_b32_e32 v6, 4, v5
	v_lshrrev_b32_e32 v4, 26, v4
	v_bitop3_b32 v5, v6, v5, 32 bitop3:0x6c
	v_add_u32_e32 v4, v1, v4
	v_ashrrev_i32_e32 v7, 31, v5
	v_ashrrev_i32_e32 v4, 6, v4
	v_lshrrev_b32_e32 v7, 26, v7
	v_lshlrev_b32_e32 v6, 3, v4
	v_add_u32_e32 v7, v5, v7
	v_and_b32_e32 v6, -16, v6
	v_ashrrev_i32_e32 v8, 6, v7
	v_and_b32_e32 v7, 0xc0, v7
	v_add_u32_e32 v6, v8, v6
	v_sub_u32_e32 v5, v5, v7
	v_lshlrev_b32_e32 v4, 5, v4
	v_ashrrev_i16_sdwa v5, v216, sext(v5) dst_sel:DWORD dst_unused:UNUSED_PAD src0_sel:DWORD src1_sel:BYTE_0
	v_lshlrev_b32_e32 v7, 1, v6
	v_lshrrev_b32_e32 v9, 2, v6
	v_and_b32_e32 v8, 3, v8
	s_mov_b32 s4, 0xfffe0
	v_and_b32_e32 v4, 32, v4
	v_bfe_i32 v5, v5, 0, 16
	v_and_b32_e32 v7, 24, v7
	v_and_b32_e32 v9, 4, v9
	v_and_or_b32 v6, v6, s4, v8
	v_or3_b32 v6, v6, v9, v7
	v_add_lshl_u32 v4, v4, v5, 1
	v_add_u32_e32 v2, 0x2000, v2
	v_lshl_add_u32 v204, v6, 12, v4
	v_ashrrev_i32_e32 v4, 31, v2
	v_lshrrev_b32_e32 v4, 22, v4
	v_add_u32_e32 v4, v2, v4
	v_ashrrev_i32_e32 v4, 10, v4
	v_mul_i32_i24_e32 v5, 0x400, v4
	v_sub_u32_e32 v2, v2, v5
	v_lshrrev_b32_e32 v5, 4, v2
	v_bitop3_b32 v2, v5, v2, 32 bitop3:0x6c
	v_ashrrev_i32_e32 v6, 31, v2
	v_lshrrev_b32_e32 v6, 26, v6
	v_lshlrev_b32_e32 v5, 3, v4
	v_add_u32_e32 v6, v2, v6
	v_and_b32_e32 v5, -16, v5
	v_ashrrev_i32_e32 v7, 6, v6
	v_and_b32_e32 v6, 0xc0, v6
	v_add_u32_e32 v5, v7, v5
	v_sub_u32_e32 v2, v2, v6
	v_lshlrev_b32_e32 v4, 5, v4
	v_ashrrev_i16_sdwa v2, v216, sext(v2) dst_sel:DWORD dst_unused:UNUSED_PAD src0_sel:DWORD src1_sel:BYTE_0
	v_lshlrev_b32_e32 v6, 1, v5
	v_lshrrev_b32_e32 v8, 2, v5
	v_and_b32_e32 v7, 3, v7
	v_and_b32_e32 v4, 32, v4
	v_bfe_i32 v2, v2, 0, 16
	v_and_b32_e32 v6, 24, v6
	v_and_b32_e32 v8, 4, v8
	v_and_or_b32 v5, v5, s4, v7
	v_or3_b32 v5, v5, v8, v6
	v_add_lshl_u32 v2, v4, v2, 1
	v_lshl_add_u32 v206, v5, 12, v2
	v_mov_b32_e32 v2, v0
	v_readlane_b32 s4, v242, 13
	v_ashrrev_i32_e32 v4, 31, v2
	v_lshrrev_b32_e32 v4, 26, v4
	v_lshlrev_b32_e32 v6, 4, v2
	v_add_u32_e32 v4, v2, v4
	v_bfe_i32 v2, v2, 27, 1
	v_lshrrev_b32_e32 v2, 22, v2
	v_add_u32_e32 v2, v6, v2
	v_and_b32_e32 v2, 0xfffffc00, v2
	v_sub_u32_e32 v2, v6, v2
	v_lshrrev_b32_e32 v5, 4, v2
	v_bitop3_b32 v2, v5, v2, 32 bitop3:0x6c
	v_ashrrev_i32_e32 v5, 31, v2
	v_lshrrev_b32_e32 v5, 26, v5
	v_ashrrev_i32_e32 v4, 6, v4
	v_add_u32_e32 v5, v2, v5
	v_ashrrev_i32_e32 v7, 6, v5
	v_lshlrev_b32_e32 v4, 5, v4
	v_and_b32_e32 v8, 32, v4
	v_and_b32_e32 v9, 0xc0, v5
	v_lshlrev_b32_e32 v5, 2, v7
	v_and_b32_e32 v4, 0xffffffc0, v4
	v_add3_u32 v4, s4, v5, v4
	ds_read2st64_b32 v[4:5], v4 offset1:2
	v_sub_u32_e32 v2, v2, v9
	v_ashrrev_i16_sdwa v2, v216, sext(v2) dst_sel:DWORD dst_unused:UNUSED_PAD src0_sel:DWORD src1_sel:BYTE_0
	v_bfe_i32 v2, v2, 0, 16
	v_add_lshl_u32 v7, v8, v2, 1
	s_waitcnt lgkmcnt(0)
	v_add_u32_e32 v2, v7, v4
	v_add_u32_e32 v4, 0x2000, v6
	v_add_u32_e32 v208, v7, v5
	v_ashrrev_i32_e32 v5, 31, v4
	v_lshrrev_b32_e32 v5, 22, v5
	v_add_u32_e32 v5, v4, v5
	v_ashrrev_i32_e32 v5, 10, v5
	v_mul_i32_i24_e32 v6, 0x400, v5
	v_sub_u32_e32 v4, v4, v6
	v_lshrrev_b32_e32 v6, 4, v4
	v_bitop3_b32 v6, v6, v4, 32 bitop3:0x6c
	v_ashrrev_i32_e32 v4, 31, v6
	v_lshrrev_b32_e32 v4, 26, v4
	s_ashr_i32 s10, s7, 6
	v_add_u32_e32 v4, v6, v4
	s_lshl_b32 s25, s10, 10
	v_ashrrev_i32_e32 v7, 6, v4
	v_lshlrev_b32_e32 v5, 5, v5
	v_and_b32_e32 v8, 32, v5
	v_and_b32_e32 v9, 0xc0, v4
	v_lshlrev_b32_e32 v4, 2, v7
	v_and_b32_e32 v5, 0xffffffc0, v5
	s_add_i32 s26, s25, 0
	s_ashr_i32 s11, s7, 8
	v_add3_u32 v4, s4, v4, v5
	s_add_i32 s27, s26, 0x10000
	s_add_i32 s28, s26, 0x12000
	ds_read2st64_b32 v[4:5], v4 offset1:2
	s_waitcnt lgkmcnt(0)
	s_mov_b32 m0, s27
	s_add_u32 s8, s16, 0x80000
	v_sub_u32_e32 v6, v6, v9
	global_load_lds_dwordx4 v204, s[16:17]
	s_mov_b32 m0, s28
	s_addc_u32 s9, s17, 0
	s_add_i32 s29, s26, 0x14000
	v_ashrrev_i16_sdwa v6, v216, sext(v6) dst_sel:DWORD dst_unused:UNUSED_PAD src0_sel:DWORD src1_sel:BYTE_0
	global_load_lds_dwordx4 v206, s[16:17]
	s_mov_b32 m0, s29
	s_add_i32 s30, s26, 0x16000
	v_bfe_i32 v6, v6, 0, 16
	global_load_lds_dwordx4 v204, s[8:9]
	s_mov_b32 m0, s30
	v_add_lshl_u32 v6, v8, v6, 1
	global_load_lds_dwordx4 v206, s[8:9]
	s_mov_b32 m0, s26
	s_add_i32 s31, s26, 0x2000
	s_waitcnt lgkmcnt(0)
	v_add_u32_e32 v210, v6, v4
	global_load_lds_dwordx4 v2, s[2:3]
	s_mov_b32 m0, s31
	s_add_i32 s34, s26, 0x4000
	global_load_lds_dwordx4 v210, s[2:3]
	s_mov_b32 m0, s34
	s_add_i32 s35, s26, 0x6000
	v_add_u32_e32 v212, v6, v5
	global_load_lds_dwordx4 v208, s[2:3]
	s_mov_b32 m0, s35
	v_mov_b32_e32 v205, v3
	global_load_lds_dwordx4 v212, s[2:3]
	v_mov_b32_e32 v207, v3
	v_mov_b32_e32 v211, v3
	s_cmp_eq_u32 s11, 1
	v_lshl_add_u64 v[10:11], s[16:17], 0, v[204:205]
	v_lshl_add_u64 v[8:9], s[16:17], 0, v[206:207]
	v_lshl_add_u64 v[4:5], s[2:3], 0, v[2:3]
	s_cselect_b64 s[8:9], -1, 0
	s_cmp_lg_u32 s11, 1
	v_lshl_add_u64 v[6:7], s[2:3], 0, v[210:211]
	s_cbranch_scc1 .LBB0_2108
	s_barrier
	s_setprio 1

.LBB0_2116:
	s_waitcnt vmcnt(8)
	s_add_u32 s20, s16, 0x80
	s_waitcnt lgkmcnt(0)
	s_addc_u32 s21, s17, 0
	s_and_b64 s[18:19], s[18:19], exec
	s_cselect_b32 s21, s7, s21
	s_cselect_b32 s20, s45, s20
	s_cselect_b32 s19, s46, s53
	s_cselect_b32 s18, s48, s52
	s_barrier
	s_nop 0
	s_waitcnt lgkmcnt(0)
	v_mfma_f32_16x16x32_bf16 v[128:131], v[148:151], v[188:191], v[128:131]
	v_mfma_f32_16x16x32_bf16 v[120:123], v[156:159], v[188:191], v[120:123]
	v_mfma_f32_16x16x32_bf16 v[112:115], v[148:151], v[180:183], v[112:115]
	v_mfma_f32_16x16x32_bf16 v[104:107], v[156:159], v[180:183], v[104:107]
	v_mfma_f32_16x16x32_bf16 v[96:99], v[148:151], v[172:175], v[96:99]
	v_mfma_f32_16x16x32_bf16 v[88:91], v[156:159], v[172:175], v[88:91]
	v_mfma_f32_16x16x32_bf16 v[80:83], v[148:151], v[164:167], v[80:83]
	v_mfma_f32_16x16x32_bf16 v[72:75], v[156:159], v[164:167], v[72:75]
	v_mfma_f32_16x16x32_bf16 v[128:131], v[152:155], v[192:195], v[128:131]
	v_mfma_f32_16x16x32_bf16 v[120:123], v[160:163], v[192:195], v[120:123]
	v_mfma_f32_16x16x32_bf16 v[112:115], v[152:155], v[184:187], v[112:115]
	v_mfma_f32_16x16x32_bf16 v[104:107], v[160:163], v[184:187], v[104:107]
	v_mfma_f32_16x16x32_bf16 v[96:99], v[152:155], v[176:179], v[96:99]
	v_mfma_f32_16x16x32_bf16 v[88:91], v[160:163], v[176:179], v[88:91]
	v_mfma_f32_16x16x32_bf16 v[80:83], v[152:155], v[168:171], v[80:83]
	v_mfma_f32_16x16x32_bf16 v[72:75], v[160:163], v[168:171], v[72:75]
	s_nop 0
	s_nop 0
	v_mfma_f32_16x16x32_bf16 v[124:127], v[132:135], v[188:191], v[124:127]
	v_mfma_f32_16x16x32_bf16 v[116:119], v[140:143], v[188:191], v[116:119]
	v_mfma_f32_16x16x32_bf16 v[108:111], v[132:135], v[180:183], v[108:111]
	v_mfma_f32_16x16x32_bf16 v[100:103], v[140:143], v[180:183], v[100:103]
	v_mfma_f32_16x16x32_bf16 v[92:95], v[132:135], v[172:175], v[92:95]
	v_mfma_f32_16x16x32_bf16 v[84:87], v[140:143], v[172:175], v[84:87]
	v_mfma_f32_16x16x32_bf16 v[76:79], v[132:135], v[164:167], v[76:79]
	v_mfma_f32_16x16x32_bf16 v[68:71], v[140:143], v[164:167], v[68:71]
	v_mfma_f32_16x16x32_bf16 v[124:127], v[136:139], v[192:195], v[124:127]
	v_mfma_f32_16x16x32_bf16 v[116:119], v[144:147], v[192:195], v[116:119]
	v_mfma_f32_16x16x32_bf16 v[108:111], v[136:139], v[184:187], v[108:111]
	v_mfma_f32_16x16x32_bf16 v[100:103], v[144:147], v[184:187], v[100:103]
	v_mfma_f32_16x16x32_bf16 v[92:95], v[136:139], v[176:179], v[92:95]
	v_mfma_f32_16x16x32_bf16 v[84:87], v[144:147], v[176:179], v[84:87]
	v_mfma_f32_16x16x32_bf16 v[76:79], v[136:139], v[168:171], v[76:79]
	v_mfma_f32_16x16x32_bf16 v[68:71], v[144:147], v[168:171], v[68:71]
	s_nop 0
	s_barrier
	s_mov_b32 m0, s27
	v_lshl_add_u64 v[228:229], s[18:19], 0, v[204:205]
	s_add_u32 s56, s18, 0x80000
	ds_read_b128 v[164:167], v226 offset:16384
	ds_read_b128 v[168:171], v226 offset:17408
	ds_read_b128 v[172:175], v226 offset:18432
	ds_read_b128 v[176:179], v226 offset:19456
	ds_read_b128 v[180:183], v226 offset:20480
	ds_read_b128 v[184:187], v226 offset:21504
	ds_read_b128 v[188:191], v226 offset:22528
	ds_read_b128 v[192:195], v226 offset:23552
	global_load_lds_dwordx4 v[228:229], off
	v_lshl_add_u64 v[230:231], s[18:19], 0, v[206:207]
	s_mov_b32 m0, s28
	s_addc_u32 s57, s19, 0
	global_load_lds_dwordx4 v[230:231], off
	v_lshl_add_u64 v[232:233], s[56:57], 0, v[204:205]
	s_mov_b32 m0, s29
	v_mov_b32_e32 v211, v3
	global_load_lds_dwordx4 v[232:233], off
	v_lshl_add_u64 v[232:233], s[56:57], 0, v[206:207]
	s_mov_b32 m0, s30
	v_lshl_add_u64 v[234:235], s[20:21], 0, v[210:211]
	global_load_lds_dwordx4 v[232:233], off
	s_mov_b32 m0, s26
	v_lshl_add_u64 v[232:233], s[20:21], 0, v[2:3]
	global_load_lds_dwordx4 v2, s[20:21]
	s_mov_b32 m0, s31
	s_nop 0
	global_load_lds_dwordx4 v210, s[20:21]
	s_waitcnt vmcnt(8)
	s_waitcnt lgkmcnt(0)
	s_barrier
	s_nop 0
	s_waitcnt lgkmcnt(0)
	v_mfma_f32_16x16x32_bf16 v[64:67], v[148:151], v[164:167], v[64:67]
	v_mfma_f32_16x16x32_bf16 v[56:59], v[156:159], v[164:167], v[56:59]
	v_mfma_f32_16x16x32_bf16 v[48:51], v[148:151], v[172:175], v[48:51]
	v_mfma_f32_16x16x32_bf16 v[40:43], v[156:159], v[172:175], v[40:43]
	v_mfma_f32_16x16x32_bf16 v[32:35], v[148:151], v[180:183], v[32:35]
	v_mfma_f32_16x16x32_bf16 v[24:27], v[156:159], v[180:183], v[24:27]
	v_mfma_f32_16x16x32_bf16 v[16:19], v[148:151], v[188:191], v[16:19]
	v_mfma_f32_16x16x32_bf16 v[8:11], v[156:159], v[188:191], v[8:11]
	v_mfma_f32_16x16x32_bf16 v[64:67], v[152:155], v[168:171], v[64:67]
	v_mfma_f32_16x16x32_bf16 v[56:59], v[160:163], v[168:171], v[56:59]
	v_mfma_f32_16x16x32_bf16 v[48:51], v[152:155], v[176:179], v[48:51]
	v_mfma_f32_16x16x32_bf16 v[40:43], v[160:163], v[176:179], v[40:43]
	v_mfma_f32_16x16x32_bf16 v[32:35], v[152:155], v[184:187], v[32:35]
	v_mfma_f32_16x16x32_bf16 v[24:27], v[160:163], v[184:187], v[24:27]
	v_mfma_f32_16x16x32_bf16 v[16:19], v[152:155], v[192:195], v[16:19]
	v_mfma_f32_16x16x32_bf16 v[8:11], v[160:163], v[192:195], v[8:11]
	s_nop 0
	s_nop 0
	v_mfma_f32_16x16x32_bf16 v[60:63], v[132:135], v[164:167], v[60:63]
	v_mfma_f32_16x16x32_bf16 v[52:55], v[140:143], v[164:167], v[52:55]
	v_mfma_f32_16x16x32_bf16 v[44:47], v[132:135], v[172:175], v[44:47]
	v_mfma_f32_16x16x32_bf16 v[36:39], v[140:143], v[172:175], v[36:39]
	v_mfma_f32_16x16x32_bf16 v[28:31], v[132:135], v[180:183], v[28:31]
	v_mfma_f32_16x16x32_bf16 v[20:23], v[140:143], v[180:183], v[20:23]
	v_mfma_f32_16x16x32_bf16 v[12:15], v[132:135], v[188:191], v[12:15]
	v_mfma_f32_16x16x32_bf16 v[4:7], v[140:143], v[188:191], v[4:7]
	v_mfma_f32_16x16x32_bf16 v[60:63], v[136:139], v[168:171], v[60:63]
	v_mfma_f32_16x16x32_bf16 v[52:55], v[144:147], v[168:171], v[52:55]
	v_mfma_f32_16x16x32_bf16 v[44:47], v[136:139], v[176:179], v[44:47]
	v_mfma_f32_16x16x32_bf16 v[36:39], v[144:147], v[176:179], v[36:39]
	v_mfma_f32_16x16x32_bf16 v[28:31], v[136:139], v[184:187], v[28:31]
	v_mfma_f32_16x16x32_bf16 v[20:23], v[144:147], v[184:187], v[20:23]
	v_mfma_f32_16x16x32_bf16 v[12:15], v[136:139], v[192:195], v[12:15]
	v_mfma_f32_16x16x32_bf16 v[4:7], v[144:147], v[192:195], v[4:7]
	s_nop 0
	s_barrier
	s_add_i32 s55, 0, 0x18000
	s_add_i32 s56, 0, 0x1c000
	v_add_u32_e32 v144, s55, v1
	v_add_u32_e32 v160, s56, v1
	ds_read_b128 v[132:135], v144
	ds_read_b128 v[136:139], v144 offset:1024
	ds_read_b128 v[140:143], v144 offset:2048
	ds_read_b128 v[144:147], v144 offset:3072
	ds_read_b128 v[148:151], v160
	ds_read_b128 v[152:155], v160 offset:1024
	ds_read_b128 v[156:159], v160 offset:2048
	ds_read_b128 v[160:163], v160 offset:3072
	s_mov_b32 m0, s34
	v_lshl_add_u64 v[214:215], s[20:21], 0, v[214:215]
	ds_read_b128 v[164:167], v226 offset:32768
	ds_read_b128 v[168:171], v226 offset:33792
	ds_read_b128 v[172:175], v226 offset:34816
	ds_read_b128 v[176:179], v226 offset:35840
	ds_read_b128 v[180:183], v226 offset:36864
	ds_read_b128 v[184:187], v226 offset:37888
	ds_read_b128 v[188:191], v226 offset:38912
	ds_read_b128 v[192:195], v226 offset:39936
	global_load_lds_dwordx4 v[214:215], off
	v_lshl_add_u64 v[214:215], s[20:21], 0, v[212:213]
	s_mov_b32 m0, s35
	s_nop 0
	global_load_lds_dwordx4 v[214:215], off
	s_waitcnt vmcnt(8)
	s_waitcnt lgkmcnt(0)
	s_barrier
	s_nop 0
	s_waitcnt lgkmcnt(0)
	v_mfma_f32_16x16x32_bf16 v[128:131], v[132:135], v[164:167], v[128:131]
	v_mfma_f32_16x16x32_bf16 v[120:123], v[140:143], v[164:167], v[120:123]
	v_mfma_f32_16x16x32_bf16 v[112:115], v[132:135], v[172:175], v[112:115]
	v_mfma_f32_16x16x32_bf16 v[104:107], v[140:143], v[172:175], v[104:107]
	v_mfma_f32_16x16x32_bf16 v[96:99], v[132:135], v[180:183], v[96:99]
	v_mfma_f32_16x16x32_bf16 v[88:91], v[140:143], v[180:183], v[88:91]
	v_mfma_f32_16x16x32_bf16 v[80:83], v[132:135], v[188:191], v[80:83]
	v_mfma_f32_16x16x32_bf16 v[72:75], v[140:143], v[188:191], v[72:75]
	v_mfma_f32_16x16x32_bf16 v[128:131], v[136:139], v[168:171], v[128:131]
	v_mfma_f32_16x16x32_bf16 v[120:123], v[144:147], v[168:171], v[120:123]
	v_mfma_f32_16x16x32_bf16 v[112:115], v[136:139], v[176:179], v[112:115]
	v_mfma_f32_16x16x32_bf16 v[104:107], v[144:147], v[176:179], v[104:107]
	v_mfma_f32_16x16x32_bf16 v[96:99], v[136:139], v[184:187], v[96:99]
	v_mfma_f32_16x16x32_bf16 v[88:91], v[144:147], v[184:187], v[88:91]
	v_mfma_f32_16x16x32_bf16 v[80:83], v[136:139], v[192:195], v[80:83]
	v_mfma_f32_16x16x32_bf16 v[72:75], v[144:147], v[192:195], v[72:75]
	s_nop 0
	s_nop 0
	v_mfma_f32_16x16x32_bf16 v[124:127], v[148:151], v[164:167], v[124:127]
	v_mfma_f32_16x16x32_bf16 v[116:119], v[156:159], v[164:167], v[116:119]
	v_mfma_f32_16x16x32_bf16 v[108:111], v[148:151], v[172:175], v[108:111]
	v_mfma_f32_16x16x32_bf16 v[100:103], v[156:159], v[172:175], v[100:103]
	v_mfma_f32_16x16x32_bf16 v[92:95], v[148:151], v[180:183], v[92:95]
	v_mfma_f32_16x16x32_bf16 v[84:87], v[156:159], v[180:183], v[84:87]
	v_mfma_f32_16x16x32_bf16 v[76:79], v[148:151], v[188:191], v[76:79]
	v_mfma_f32_16x16x32_bf16 v[68:71], v[156:159], v[188:191], v[68:71]
	v_mfma_f32_16x16x32_bf16 v[124:127], v[152:155], v[168:171], v[124:127]
	v_mfma_f32_16x16x32_bf16 v[116:119], v[160:163], v[168:171], v[116:119]
	v_mfma_f32_16x16x32_bf16 v[108:111], v[152:155], v[176:179], v[108:111]
	v_mfma_f32_16x16x32_bf16 v[100:103], v[160:163], v[176:179], v[100:103]
	v_mfma_f32_16x16x32_bf16 v[92:95], v[152:155], v[184:187], v[92:95]
	v_mfma_f32_16x16x32_bf16 v[84:87], v[160:163], v[184:187], v[84:87]
	v_mfma_f32_16x16x32_bf16 v[76:79], v[152:155], v[192:195], v[76:79]
	v_mfma_f32_16x16x32_bf16 v[68:71], v[160:163], v[192:195], v[68:71]
	s_nop 0
	s_barrier
	s_add_i32 s20, s55, s25
	v_lshl_add_u64 v[214:215], v[228:229], 0, s[94:95]
	s_mov_b32 m0, s20
	ds_read_b128 v[164:167], v226 offset:49152
	ds_read_b128 v[168:171], v226 offset:50176
	ds_read_b128 v[172:175], v226 offset:51200
	ds_read_b128 v[176:179], v226 offset:52224
	ds_read_b128 v[180:183], v226 offset:53248
	ds_read_b128 v[184:187], v226 offset:54272
	ds_read_b128 v[188:191], v226 offset:55296
	ds_read_b128 v[192:195], v226 offset:56320
	global_load_lds_dwordx4 v[214:215], off
	s_add_i32 m0, s20, 0x2000
	s_add_u32 s18, s18, 0x80080
	v_lshl_add_u64 v[214:215], v[230:231], 0, s[94:95]
	s_addc_u32 s19, s19, 0
	s_add_i32 s20, s56, s25
	global_load_lds_dwordx4 v[214:215], off
	v_lshl_add_u64 v[214:215], s[18:19], 0, v[204:205]
	s_mov_b32 m0, s20
	s_nop 0
	global_load_lds_dwordx4 v[214:215], off
	v_lshl_add_u64 v[214:215], s[18:19], 0, v[206:207]
	s_add_i32 m0, s20, 0x2000
	s_nop 0
	global_load_lds_dwordx4 v[214:215], off
	v_lshl_add_u64 v[214:215], v[232:233], 0, s[94:95]
	s_mov_b32 m0, s38
	s_nop 0
	global_load_lds_dwordx4 v[214:215], off
	v_lshl_add_u64 v[214:215], v[234:235], 0, s[94:95]
	s_mov_b32 m0, s39
	s_nop 0
	global_load_lds_dwordx4 v[214:215], off
	s_waitcnt vmcnt(8)
	s_waitcnt lgkmcnt(0)
	s_barrier
	s_nop 0
	s_waitcnt lgkmcnt(0)
	v_mfma_f32_16x16x32_bf16 v[64:67], v[132:135], v[164:167], v[64:67]
	v_mfma_f32_16x16x32_bf16 v[56:59], v[140:143], v[164:167], v[56:59]
	v_mfma_f32_16x16x32_bf16 v[48:51], v[132:135], v[172:175], v[48:51]
	v_mfma_f32_16x16x32_bf16 v[40:43], v[140:143], v[172:175], v[40:43]
	v_mfma_f32_16x16x32_bf16 v[32:35], v[132:135], v[180:183], v[32:35]
	v_mfma_f32_16x16x32_bf16 v[24:27], v[140:143], v[180:183], v[24:27]
	v_mfma_f32_16x16x32_bf16 v[16:19], v[132:135], v[188:191], v[16:19]
	v_mfma_f32_16x16x32_bf16 v[8:11], v[140:143], v[188:191], v[8:11]
	v_mfma_f32_16x16x32_bf16 v[64:67], v[136:139], v[168:171], v[64:67]
	v_mfma_f32_16x16x32_bf16 v[56:59], v[144:147], v[168:171], v[56:59]
	v_mfma_f32_16x16x32_bf16 v[48:51], v[136:139], v[176:179], v[48:51]
	v_mfma_f32_16x16x32_bf16 v[40:43], v[144:147], v[176:179], v[40:43]
	v_mfma_f32_16x16x32_bf16 v[32:35], v[136:139], v[184:187], v[32:35]
	v_mfma_f32_16x16x32_bf16 v[24:27], v[144:147], v[184:187], v[24:27]
	v_mfma_f32_16x16x32_bf16 v[16:19], v[136:139], v[192:195], v[16:19]
	v_mfma_f32_16x16x32_bf16 v[8:11], v[144:147], v[192:195], v[8:11]
	s_nop 0
	s_nop 0
	v_mfma_f32_16x16x32_bf16 v[60:63], v[148:151], v[164:167], v[60:63]
	v_mfma_f32_16x16x32_bf16 v[52:55], v[156:159], v[164:167], v[52:55]
	v_mfma_f32_16x16x32_bf16 v[44:47], v[148:151], v[172:175], v[44:47]
	v_mfma_f32_16x16x32_bf16 v[36:39], v[156:159], v[172:175], v[36:39]
	v_mfma_f32_16x16x32_bf16 v[28:31], v[148:151], v[180:183], v[28:31]
	v_mfma_f32_16x16x32_bf16 v[20:23], v[156:159], v[180:183], v[20:23]
	v_mfma_f32_16x16x32_bf16 v[12:15], v[148:151], v[188:191], v[12:15]
	v_mfma_f32_16x16x32_bf16 v[4:7], v[156:159], v[188:191], v[4:7]
	v_mfma_f32_16x16x32_bf16 v[60:63], v[152:155], v[168:171], v[60:63]
	v_mfma_f32_16x16x32_bf16 v[52:55], v[160:163], v[168:171], v[52:55]
	v_mfma_f32_16x16x32_bf16 v[44:47], v[152:155], v[176:179], v[44:47]
	v_mfma_f32_16x16x32_bf16 v[36:39], v[160:163], v[176:179], v[36:39]
	v_mfma_f32_16x16x32_bf16 v[28:31], v[152:155], v[184:187], v[28:31]
	v_mfma_f32_16x16x32_bf16 v[20:23], v[160:163], v[184:187], v[20:23]
	v_mfma_f32_16x16x32_bf16 v[12:15], v[152:155], v[192:195], v[12:15]
	v_mfma_f32_16x16x32_bf16 v[4:7], v[160:163], v[192:195], v[4:7]
	s_nop 0
	s_barrier
	s_add_i32 s54, s54, 2
	s_add_u32 s52, s52, 0x100
	s_addc_u32 s53, s53, 0
	s_add_u32 s16, s16, 0x100
	s_addc_u32 s17, s17, 0
	s_cmp_gt_u32 s54, 29
	s_cbranch_scc1 .LBB0_2119

.LBB0_2141:
	s_add_i32 s18, s91, 7
	s_cmp_ge_i32 s18, s67
	s_waitcnt vmcnt(0) lgkmcnt(0)
	s_barrier
	s_cbranch_scc1 .LBB0_2190
	s_waitcnt vmcnt(0)
	s_barrier
	s_setprio 0
	s_mov_b64 s[2:3], exec
	v_readlane_b32 s4, v243, 59
	v_readlane_b32 s5, v243, 60
	s_and_b64 s[4:5], s[2:3], s[4:5]
	s_mov_b64 exec, s[4:5]
	s_cbranch_execz .LBB0_2189
	v_readlane_b32 s4, v243, 56
	s_waitcnt vmcnt(0) expcnt(0) lgkmcnt(0)
	s_nop 0
	v_mov_b32_e32 v1, s4
	ds_read_b32 v4, v1
	ds_read_b32 v2, v1 offset:4
	s_waitcnt lgkmcnt(1)
	v_cmp_ne_u32_e32 vcc, 0, v4
	s_cbranch_vccnz .LBB0_2157
	s_load_dwordx2 s[4:5], s[0:1], 0x0
	s_load_dword s6, s[0:1], 0x8
	s_mov_b32 s10, 0
	s_waitcnt lgkmcnt(0)
	s_mul_i32 s9, s5, s4
	s_mul_i32 s9, s9, s6
	s_branch .LBB0_2146

.LBB0_2663:
	s_andn2_b64 vcc, exec, s[2:3]
	s_cbranch_vccnz .LBB0_2701
	v_bfe_i32 v5, v1, 27, 1
	v_lshlrev_b32_e32 v2, 4, v1
	v_lshrrev_b32_e32 v5, 22, v5
	v_add_u32_e32 v5, v2, v5
	v_and_b32_e32 v5, 0xfffffc00, v5
	v_sub_u32_e32 v5, v2, v5
	v_ashrrev_i32_e32 v4, 31, v1
	v_lshrrev_b32_e32 v6, 4, v5
	v_lshrrev_b32_e32 v4, 26, v4
	v_bitop3_b32 v5, v6, v5, 32 bitop3:0x6c
	v_add_u32_e32 v4, v1, v4
	v_ashrrev_i32_e32 v7, 31, v5
	v_ashrrev_i32_e32 v4, 6, v4
	v_lshrrev_b32_e32 v7, 26, v7
	v_lshlrev_b32_e32 v6, 3, v4
	v_add_u32_e32 v7, v5, v7
	v_and_b32_e32 v6, -16, v6
	v_ashrrev_i32_e32 v8, 6, v7
	v_and_b32_e32 v7, 0xc0, v7
	v_add_u32_e32 v6, v8, v6
	v_sub_u32_e32 v5, v5, v7
	v_lshlrev_b32_e32 v4, 5, v4
	v_ashrrev_i16_sdwa v5, v216, sext(v5) dst_sel:DWORD dst_unused:UNUSED_PAD src0_sel:DWORD src1_sel:BYTE_0
	v_lshlrev_b32_e32 v7, 1, v6
	v_lshrrev_b32_e32 v9, 2, v6
	v_and_b32_e32 v8, 3, v8
	s_mov_b32 s2, 0x7fffe0
	v_and_b32_e32 v4, 32, v4
	v_bfe_i32 v5, v5, 0, 16
	v_and_b32_e32 v7, 24, v7
	v_and_b32_e32 v9, 4, v9
	v_and_or_b32 v8, v6, s2, v8
	v_or3_b32 v7, v8, v9, v7
	v_add_lshl_u32 v4, v4, v5, 1
	v_add_u32_e32 v2, 0x2000, v2
	v_lshl_add_u32 v136, v7, 9, v4
	v_lshl_add_u32 v138, v6, 9, v4
	v_ashrrev_i32_e32 v4, 31, v2
	v_lshrrev_b32_e32 v4, 22, v4
	v_add_u32_e32 v4, v2, v4
	v_ashrrev_i32_e32 v4, 10, v4
	v_mul_i32_i24_e32 v5, 0x400, v4
	v_sub_u32_e32 v2, v2, v5
	v_lshrrev_b32_e32 v5, 4, v2
	v_bitop3_b32 v2, v5, v2, 32 bitop3:0x6c
	v_ashrrev_i32_e32 v6, 31, v2
	v_lshrrev_b32_e32 v6, 26, v6
	v_lshlrev_b32_e32 v5, 3, v4
	v_add_u32_e32 v6, v2, v6
	s_ashr_i32 s8, s9, 6
	v_and_b32_e32 v5, -16, v5
	v_ashrrev_i32_e32 v7, 6, v6
	v_and_b32_e32 v6, 0xc0, v6
	v_add_u32_e32 v5, v7, v5
	v_sub_u32_e32 v2, v2, v6
	s_lshl_b32 s53, s8, 10
	v_lshlrev_b32_e32 v4, 5, v4
	v_ashrrev_i16_sdwa v2, v216, sext(v2) dst_sel:DWORD dst_unused:UNUSED_PAD src0_sel:DWORD src1_sel:BYTE_0
	v_lshlrev_b32_e32 v6, 1, v5
	v_lshrrev_b32_e32 v8, 2, v5
	v_and_b32_e32 v7, 3, v7
	s_add_i32 s54, s53, 0
	v_and_b32_e32 v4, 32, v4
	v_bfe_i32 v2, v2, 0, 16
	v_and_b32_e32 v6, 24, v6
	v_and_b32_e32 v8, 4, v8
	v_and_or_b32 v7, v5, s2, v7
	s_waitcnt lgkmcnt(0)
	s_add_i32 m0, s54, 0x10000
	v_or3_b32 v6, v7, v8, v6
	v_add_lshl_u32 v2, v4, v2, 1
	s_ashr_i32 s12, s9, 8
	global_load_lds_dwordx4 v136, s[28:29]
	s_add_i32 m0, s54, 0x12000
	v_lshl_add_u32 v140, v6, 9, v2
	s_add_u32 s2, s28, 0x10000
	global_load_lds_dwordx4 v140, s[28:29]
	s_addc_u32 s3, s29, 0
	s_add_i32 m0, s54, 0x14000
	s_add_i32 s55, s54, 0x2000
	global_load_lds_dwordx4 v136, s[2:3]
	s_add_i32 m0, s54, 0x16000
	v_lshl_add_u32 v142, v5, 9, v2
	global_load_lds_dwordx4 v140, s[2:3]
	s_mov_b32 m0, s54
	s_add_u32 s2, s26, 0x10000
	global_load_lds_dwordx4 v138, s[26:27]
	s_mov_b32 m0, s55
	s_addc_u32 s3, s27, 0
	s_add_i32 s56, s54, 0x4000
	global_load_lds_dwordx4 v142, s[26:27]
	s_mov_b32 m0, s56
	s_add_i32 s57, s54, 0x6000
	global_load_lds_dwordx4 v138, s[2:3]
	s_mov_b32 m0, s57
	v_mov_b32_e32 v137, v3
	global_load_lds_dwordx4 v142, s[2:3]
	v_mov_b32_e32 v141, v3
	v_mov_b32_e32 v139, v3
	v_mov_b32_e32 v143, v3
	s_cmp_eq_u32 s12, 1
	v_lshl_add_u64 v[10:11], s[28:29], 0, v[136:137]
	v_lshl_add_u64 v[8:9], s[28:29], 0, v[140:141]
	v_lshl_add_u64 v[4:5], s[26:27], 0, v[138:139]
	s_cselect_b64 s[2:3], -1, 0
	s_cmp_lg_u32 s12, 1
	v_lshl_add_u64 v[6:7], s[26:27], 0, v[142:143]
	s_cbranch_scc1 .LBB0_2666
	s_barrier
	s_setprio 1

.LBB0_2674:
	s_add_u32 s40, s26, s34
	s_addc_u32 s41, s27, s35
	s_add_u32 s38, s40, 0x100
	s_addc_u32 s39, s41, 0
	v_cndmask_b32_e64 v2, 0, 1, s[36:37]
	s_and_b64 s[36:37], s[30:31], exec
	s_cselect_b32 s37, s19, s39
	s_cselect_b32 s36, s25, s38
	s_add_u32 s34, s28, s34
	s_addc_u32 s35, s29, s35
	s_add_u32 s34, s34, 0x100
	s_addc_u32 s35, s35, 0
	s_add_i32 s73, 0, 0x10000
	s_and_b64 s[30:31], s[30:31], exec
	s_cselect_b32 s39, s46, s35
	s_cselect_b32 s38, s64, s34
	s_add_i32 s31, 0, 0x14000
	s_add_u32 s42, s40, 0x10080
	s_addc_u32 s43, s41, 0
	s_add_i32 s72, s73, s53
	s_add_i32 m0, s54, 0xc000
	s_add_i32 s76, s54, 0xe000
	s_add_i32 s69, s72, 0x2000
	v_add_u32_e32 v144, s73, v1
	s_add_u32 s40, s38, 0x10000
	ds_read_b128 v[132:135], v144
	ds_read_b128 v[148:151], v144 offset:1024
	ds_read_b128 v[152:155], v144 offset:2048
	ds_read_b128 v[156:159], v144 offset:3072
	v_add_u32_e32 v144, s31, v1
	s_addc_u32 s41, s39, 0
	s_add_i32 s71, s31, s53
	ds_read_b128 v[160:163], v144
	ds_read_b128 v[164:167], v144 offset:1024
	ds_read_b128 v[168:171], v144 offset:2048
	ds_read_b128 v[172:175], v144 offset:3072
	s_add_i32 s70, s71, 0x2000
	s_add_i32 s68, 0, 0x18000
	s_add_i32 s67, 0, 0x1c000
	s_add_u32 s34, s36, 0x10000
	s_addc_u32 s35, s37, 0
	s_add_i32 s66, s68, s53
	s_add_i32 s65, s66, 0x2000
	s_add_u32 s30, s38, 0x10080
	s_addc_u32 s31, s39, 0
	s_add_i32 s75, s67, s53
	s_add_i32 s73, s75, 0x2000
	v_cmp_ne_u32_e32 vcc, 1, v2
	v_lshl_add_u64 v[144:145], s[42:43], 0, v[138:139]
	ds_read_b128 v[176:179], v146
	ds_read_b128 v[180:183], v146 offset:1024
	ds_read_b128 v[184:187], v146 offset:2048
	ds_read_b128 v[188:191], v146 offset:3072
	ds_read_b128 v[192:195], v146 offset:4096
	ds_read_b128 v[204:207], v146 offset:5120
	ds_read_b128 v[208:211], v146 offset:6144
	ds_read_b128 v[212:215], v146 offset:7168
	global_load_lds_dwordx4 v[144:145], off
	v_lshl_add_u64 v[144:145], s[42:43], 0, v[142:143]
	s_mov_b32 m0, s76
	s_nop 0
	global_load_lds_dwordx4 v[144:145], off
	s_waitcnt vmcnt(8)
	s_waitcnt lgkmcnt(0)
	s_barrier
	s_nop 0
	s_waitcnt lgkmcnt(0)
	v_mfma_f32_16x16x32_bf16 v[128:131], v[132:135], v[176:179], v[128:131]
	v_mfma_f32_16x16x32_bf16 v[124:127], v[152:155], v[176:179], v[124:127]
	v_mfma_f32_16x16x32_bf16 v[116:119], v[132:135], v[184:187], v[116:119]
	v_mfma_f32_16x16x32_bf16 v[108:111], v[152:155], v[184:187], v[108:111]
	v_mfma_f32_16x16x32_bf16 v[100:103], v[132:135], v[192:195], v[100:103]
	v_mfma_f32_16x16x32_bf16 v[92:95], v[152:155], v[192:195], v[92:95]
	v_mfma_f32_16x16x32_bf16 v[84:87], v[132:135], v[208:211], v[84:87]
	v_mfma_f32_16x16x32_bf16 v[76:79], v[152:155], v[208:211], v[76:79]
	v_mfma_f32_16x16x32_bf16 v[128:131], v[148:151], v[180:183], v[128:131]
	v_mfma_f32_16x16x32_bf16 v[124:127], v[156:159], v[180:183], v[124:127]
	v_mfma_f32_16x16x32_bf16 v[116:119], v[148:151], v[188:191], v[116:119]
	v_mfma_f32_16x16x32_bf16 v[108:111], v[156:159], v[188:191], v[108:111]
	v_mfma_f32_16x16x32_bf16 v[100:103], v[148:151], v[204:207], v[100:103]
	v_mfma_f32_16x16x32_bf16 v[92:95], v[156:159], v[204:207], v[92:95]
	v_mfma_f32_16x16x32_bf16 v[84:87], v[148:151], v[212:215], v[84:87]
	v_mfma_f32_16x16x32_bf16 v[76:79], v[156:159], v[212:215], v[76:79]
	s_nop 0
	s_nop 0
	v_mfma_f32_16x16x32_bf16 v[120:123], v[160:163], v[176:179], v[120:123]
	v_mfma_f32_16x16x32_bf16 v[112:115], v[168:171], v[176:179], v[112:115]
	v_mfma_f32_16x16x32_bf16 v[104:107], v[160:163], v[184:187], v[104:107]
	v_mfma_f32_16x16x32_bf16 v[96:99], v[168:171], v[184:187], v[96:99]
	v_mfma_f32_16x16x32_bf16 v[88:91], v[160:163], v[192:195], v[88:91]
	v_mfma_f32_16x16x32_bf16 v[80:83], v[168:171], v[192:195], v[80:83]
	v_mfma_f32_16x16x32_bf16 v[72:75], v[160:163], v[208:211], v[72:75]
	v_mfma_f32_16x16x32_bf16 v[68:71], v[168:171], v[208:211], v[68:71]
	v_mfma_f32_16x16x32_bf16 v[120:123], v[164:167], v[180:183], v[120:123]
	v_mfma_f32_16x16x32_bf16 v[112:115], v[172:175], v[180:183], v[112:115]
	v_mfma_f32_16x16x32_bf16 v[104:107], v[164:167], v[188:191], v[104:107]
	v_mfma_f32_16x16x32_bf16 v[96:99], v[172:175], v[188:191], v[96:99]
	v_mfma_f32_16x16x32_bf16 v[88:91], v[164:167], v[204:207], v[88:91]
	v_mfma_f32_16x16x32_bf16 v[80:83], v[172:175], v[204:207], v[80:83]
	v_mfma_f32_16x16x32_bf16 v[72:75], v[164:167], v[212:215], v[72:75]
	v_mfma_f32_16x16x32_bf16 v[68:71], v[172:175], v[212:215], v[68:71]
	s_nop 0
	s_barrier
	s_mov_b32 m0, s72
	v_lshl_add_u64 v[144:145], s[38:39], 0, v[136:137]
	ds_read_b128 v[176:179], v146 offset:16384
	ds_read_b128 v[180:183], v146 offset:17408
	ds_read_b128 v[184:187], v146 offset:18432
	ds_read_b128 v[188:191], v146 offset:19456
	ds_read_b128 v[192:195], v146 offset:20480
	ds_read_b128 v[204:207], v146 offset:21504
	ds_read_b128 v[208:211], v146 offset:22528
	ds_read_b128 v[212:215], v146 offset:23552
	global_load_lds_dwordx4 v[144:145], off
	v_lshl_add_u64 v[226:227], s[38:39], 0, v[140:141]
	s_mov_b32 m0, s69
	v_lshl_add_u64 v[228:229], s[40:41], 0, v[136:137]
	global_load_lds_dwordx4 v[226:227], off
	s_mov_b32 m0, s71
	v_lshl_add_u64 v[230:231], s[36:37], 0, v[142:143]
	global_load_lds_dwordx4 v[228:229], off
	v_lshl_add_u64 v[228:229], s[40:41], 0, v[140:141]
	s_mov_b32 m0, s70
	s_nop 0
	global_load_lds_dwordx4 v[228:229], off
	v_lshl_add_u64 v[228:229], s[36:37], 0, v[138:139]
	s_mov_b32 m0, s54
	s_nop 0
	global_load_lds_dwordx4 v[228:229], off
	s_mov_b32 m0, s55
	s_nop 0
	global_load_lds_dwordx4 v[230:231], off
	s_waitcnt vmcnt(8)
	s_waitcnt lgkmcnt(0)
	s_barrier
	s_nop 0
	s_waitcnt lgkmcnt(0)
	v_mfma_f32_16x16x32_bf16 v[64:67], v[132:135], v[176:179], v[64:67]
	v_mfma_f32_16x16x32_bf16 v[60:63], v[152:155], v[176:179], v[60:63]
	v_mfma_f32_16x16x32_bf16 v[52:55], v[132:135], v[184:187], v[52:55]
	v_mfma_f32_16x16x32_bf16 v[44:47], v[152:155], v[184:187], v[44:47]
	v_mfma_f32_16x16x32_bf16 v[36:39], v[132:135], v[192:195], v[36:39]
	v_mfma_f32_16x16x32_bf16 v[28:31], v[152:155], v[192:195], v[28:31]
	v_mfma_f32_16x16x32_bf16 v[20:23], v[132:135], v[208:211], v[20:23]
	v_mfma_f32_16x16x32_bf16 v[12:15], v[152:155], v[208:211], v[12:15]
	v_mfma_f32_16x16x32_bf16 v[64:67], v[148:151], v[180:183], v[64:67]
	v_mfma_f32_16x16x32_bf16 v[60:63], v[156:159], v[180:183], v[60:63]
	v_mfma_f32_16x16x32_bf16 v[52:55], v[148:151], v[188:191], v[52:55]
	v_mfma_f32_16x16x32_bf16 v[44:47], v[156:159], v[188:191], v[44:47]
	v_mfma_f32_16x16x32_bf16 v[36:39], v[148:151], v[204:207], v[36:39]
	v_mfma_f32_16x16x32_bf16 v[28:31], v[156:159], v[204:207], v[28:31]
	v_mfma_f32_16x16x32_bf16 v[20:23], v[148:151], v[212:215], v[20:23]
	v_mfma_f32_16x16x32_bf16 v[12:15], v[156:159], v[212:215], v[12:15]
	s_nop 0
	s_nop 0
	v_mfma_f32_16x16x32_bf16 v[56:59], v[160:163], v[176:179], v[56:59]
	v_mfma_f32_16x16x32_bf16 v[48:51], v[168:171], v[176:179], v[48:51]
	v_mfma_f32_16x16x32_bf16 v[40:43], v[160:163], v[184:187], v[40:43]
	v_mfma_f32_16x16x32_bf16 v[32:35], v[168:171], v[184:187], v[32:35]
	v_mfma_f32_16x16x32_bf16 v[24:27], v[160:163], v[192:195], v[24:27]
	v_mfma_f32_16x16x32_bf16 v[16:19], v[168:171], v[192:195], v[16:19]
	v_mfma_f32_16x16x32_bf16 v[8:11], v[160:163], v[208:211], v[8:11]
	v_mfma_f32_16x16x32_bf16 v[4:7], v[168:171], v[208:211], v[4:7]
	v_mfma_f32_16x16x32_bf16 v[56:59], v[164:167], v[180:183], v[56:59]
	v_mfma_f32_16x16x32_bf16 v[48:51], v[172:175], v[180:183], v[48:51]
	v_mfma_f32_16x16x32_bf16 v[40:43], v[164:167], v[188:191], v[40:43]
	v_mfma_f32_16x16x32_bf16 v[32:35], v[172:175], v[188:191], v[32:35]
	v_mfma_f32_16x16x32_bf16 v[24:27], v[164:167], v[204:207], v[24:27]
	v_mfma_f32_16x16x32_bf16 v[16:19], v[172:175], v[204:207], v[16:19]
	v_mfma_f32_16x16x32_bf16 v[8:11], v[164:167], v[212:215], v[8:11]
	v_mfma_f32_16x16x32_bf16 v[4:7], v[172:175], v[212:215], v[4:7]
	s_nop 0
	s_barrier
	v_add_u32_e32 v2, s68, v1
	ds_read_b128 v[132:135], v2
	ds_read_b128 v[148:151], v2 offset:1024
	ds_read_b128 v[152:155], v2 offset:2048
	ds_read_b128 v[156:159], v2 offset:3072
	v_add_u32_e32 v2, s67, v1
	ds_read_b128 v[160:163], v2
	ds_read_b128 v[164:167], v2 offset:1024
	ds_read_b128 v[168:171], v2 offset:2048
	ds_read_b128 v[172:175], v2 offset:3072
	s_mov_b32 m0, s56
	v_lshl_add_u64 v[232:233], s[34:35], 0, v[138:139]
	ds_read_b128 v[176:179], v146 offset:32768
	ds_read_b128 v[180:183], v146 offset:33792
	ds_read_b128 v[184:187], v146 offset:34816
	ds_read_b128 v[188:191], v146 offset:35840
	ds_read_b128 v[192:195], v146 offset:36864
	ds_read_b128 v[204:207], v146 offset:37888
	ds_read_b128 v[208:211], v146 offset:38912
	ds_read_b128 v[212:215], v146 offset:39936
	global_load_lds_dwordx4 v[232:233], off
	v_lshl_add_u64 v[232:233], s[34:35], 0, v[142:143]
	s_mov_b32 m0, s57
	s_nop 0
	global_load_lds_dwordx4 v[232:233], off
	s_waitcnt vmcnt(8)
	s_waitcnt lgkmcnt(0)
	s_barrier
	s_nop 0
	s_waitcnt lgkmcnt(0)
	v_mfma_f32_16x16x32_bf16 v[128:131], v[132:135], v[176:179], v[128:131]
	v_mfma_f32_16x16x32_bf16 v[124:127], v[152:155], v[176:179], v[124:127]
	v_mfma_f32_16x16x32_bf16 v[116:119], v[132:135], v[184:187], v[116:119]
	v_mfma_f32_16x16x32_bf16 v[108:111], v[152:155], v[184:187], v[108:111]
	v_mfma_f32_16x16x32_bf16 v[100:103], v[132:135], v[192:195], v[100:103]
	v_mfma_f32_16x16x32_bf16 v[92:95], v[152:155], v[192:195], v[92:95]
	v_mfma_f32_16x16x32_bf16 v[84:87], v[132:135], v[208:211], v[84:87]
	v_mfma_f32_16x16x32_bf16 v[76:79], v[152:155], v[208:211], v[76:79]
	v_mfma_f32_16x16x32_bf16 v[128:131], v[148:151], v[180:183], v[128:131]
	v_mfma_f32_16x16x32_bf16 v[124:127], v[156:159], v[180:183], v[124:127]
	v_mfma_f32_16x16x32_bf16 v[116:119], v[148:151], v[188:191], v[116:119]
	v_mfma_f32_16x16x32_bf16 v[108:111], v[156:159], v[188:191], v[108:111]
	v_mfma_f32_16x16x32_bf16 v[100:103], v[148:151], v[204:207], v[100:103]
	v_mfma_f32_16x16x32_bf16 v[92:95], v[156:159], v[204:207], v[92:95]
	v_mfma_f32_16x16x32_bf16 v[84:87], v[148:151], v[212:215], v[84:87]
	v_mfma_f32_16x16x32_bf16 v[76:79], v[156:159], v[212:215], v[76:79]
	s_nop 0
	s_nop 0
	v_mfma_f32_16x16x32_bf16 v[120:123], v[160:163], v[176:179], v[120:123]
	v_mfma_f32_16x16x32_bf16 v[112:115], v[168:171], v[176:179], v[112:115]
	v_mfma_f32_16x16x32_bf16 v[104:107], v[160:163], v[184:187], v[104:107]
	v_mfma_f32_16x16x32_bf16 v[96:99], v[168:171], v[184:187], v[96:99]
	v_mfma_f32_16x16x32_bf16 v[88:91], v[160:163], v[192:195], v[88:91]
	v_mfma_f32_16x16x32_bf16 v[80:83], v[168:171], v[192:195], v[80:83]
	v_mfma_f32_16x16x32_bf16 v[72:75], v[160:163], v[208:211], v[72:75]
	v_mfma_f32_16x16x32_bf16 v[68:71], v[168:171], v[208:211], v[68:71]
	v_mfma_f32_16x16x32_bf16 v[120:123], v[164:167], v[180:183], v[120:123]
	v_mfma_f32_16x16x32_bf16 v[112:115], v[172:175], v[180:183], v[112:115]
	v_mfma_f32_16x16x32_bf16 v[104:107], v[164:167], v[188:191], v[104:107]
	v_mfma_f32_16x16x32_bf16 v[96:99], v[172:175], v[188:191], v[96:99]
	v_mfma_f32_16x16x32_bf16 v[88:91], v[164:167], v[204:207], v[88:91]
	v_mfma_f32_16x16x32_bf16 v[80:83], v[172:175], v[204:207], v[80:83]
	v_mfma_f32_16x16x32_bf16 v[72:75], v[164:167], v[212:215], v[72:75]
	v_mfma_f32_16x16x32_bf16 v[68:71], v[172:175], v[212:215], v[68:71]
	s_nop 0
	s_barrier
	s_mov_b32 m0, s66
	v_lshl_add_u64 v[144:145], v[144:145], 0, s[94:95]
	ds_read_b128 v[176:179], v146 offset:49152
	ds_read_b128 v[180:183], v146 offset:50176
	ds_read_b128 v[184:187], v146 offset:51200
	ds_read_b128 v[188:191], v146 offset:52224
	ds_read_b128 v[192:195], v146 offset:53248
	ds_read_b128 v[204:207], v146 offset:54272
	ds_read_b128 v[208:211], v146 offset:55296
	ds_read_b128 v[212:215], v146 offset:56320
	global_load_lds_dwordx4 v[144:145], off
	v_lshl_add_u64 v[144:145], v[226:227], 0, s[94:95]
	s_mov_b32 m0, s65
	s_nop 0
	global_load_lds_dwordx4 v[144:145], off
	v_lshl_add_u64 v[144:145], s[30:31], 0, v[136:137]
	s_mov_b32 m0, s75
	s_nop 0
	global_load_lds_dwordx4 v[144:145], off
	v_lshl_add_u64 v[144:145], s[30:31], 0, v[140:141]
	s_mov_b32 m0, s73
	s_nop 0
	global_load_lds_dwordx4 v[144:145], off
	v_lshl_add_u64 v[144:145], v[228:229], 0, s[94:95]
	s_mov_b32 m0, s59
	s_nop 0
	global_load_lds_dwordx4 v[144:145], off
	v_lshl_add_u64 v[144:145], v[230:231], 0, s[94:95]
	s_mov_b32 m0, s60
	s_nop 0
	global_load_lds_dwordx4 v[144:145], off
	s_waitcnt vmcnt(8)
	s_waitcnt lgkmcnt(0)
	s_barrier
	s_nop 0
	s_waitcnt lgkmcnt(0)
	v_mfma_f32_16x16x32_bf16 v[64:67], v[132:135], v[176:179], v[64:67]
	v_mfma_f32_16x16x32_bf16 v[60:63], v[152:155], v[176:179], v[60:63]
	v_mfma_f32_16x16x32_bf16 v[52:55], v[132:135], v[184:187], v[52:55]
	v_mfma_f32_16x16x32_bf16 v[44:47], v[152:155], v[184:187], v[44:47]
	v_mfma_f32_16x16x32_bf16 v[36:39], v[132:135], v[192:195], v[36:39]
	v_mfma_f32_16x16x32_bf16 v[28:31], v[152:155], v[192:195], v[28:31]
	v_mfma_f32_16x16x32_bf16 v[20:23], v[132:135], v[208:211], v[20:23]
	v_mfma_f32_16x16x32_bf16 v[12:15], v[152:155], v[208:211], v[12:15]
	v_mfma_f32_16x16x32_bf16 v[64:67], v[148:151], v[180:183], v[64:67]
	v_mfma_f32_16x16x32_bf16 v[60:63], v[156:159], v[180:183], v[60:63]
	v_mfma_f32_16x16x32_bf16 v[52:55], v[148:151], v[188:191], v[52:55]
	v_mfma_f32_16x16x32_bf16 v[44:47], v[156:159], v[188:191], v[44:47]
	v_mfma_f32_16x16x32_bf16 v[36:39], v[148:151], v[204:207], v[36:39]
	v_mfma_f32_16x16x32_bf16 v[28:31], v[156:159], v[204:207], v[28:31]
	v_mfma_f32_16x16x32_bf16 v[20:23], v[148:151], v[212:215], v[20:23]
	v_mfma_f32_16x16x32_bf16 v[12:15], v[156:159], v[212:215], v[12:15]
	s_nop 0
	s_nop 0
	v_mfma_f32_16x16x32_bf16 v[56:59], v[160:163], v[176:179], v[56:59]
	v_mfma_f32_16x16x32_bf16 v[48:51], v[168:171], v[176:179], v[48:51]
	v_mfma_f32_16x16x32_bf16 v[40:43], v[160:163], v[184:187], v[40:43]
	v_mfma_f32_16x16x32_bf16 v[32:35], v[168:171], v[184:187], v[32:35]
	v_mfma_f32_16x16x32_bf16 v[24:27], v[160:163], v[192:195], v[24:27]
	v_mfma_f32_16x16x32_bf16 v[16:19], v[168:171], v[192:195], v[16:19]
	v_mfma_f32_16x16x32_bf16 v[8:11], v[160:163], v[208:211], v[8:11]
	v_mfma_f32_16x16x32_bf16 v[4:7], v[168:171], v[208:211], v[4:7]
	v_mfma_f32_16x16x32_bf16 v[56:59], v[164:167], v[180:183], v[56:59]
	v_mfma_f32_16x16x32_bf16 v[48:51], v[172:175], v[180:183], v[48:51]
	v_mfma_f32_16x16x32_bf16 v[40:43], v[164:167], v[188:191], v[40:43]
	v_mfma_f32_16x16x32_bf16 v[32:35], v[172:175], v[188:191], v[32:35]
	v_mfma_f32_16x16x32_bf16 v[24:27], v[164:167], v[204:207], v[24:27]
	v_mfma_f32_16x16x32_bf16 v[16:19], v[172:175], v[204:207], v[16:19]
	v_mfma_f32_16x16x32_bf16 v[8:11], v[164:167], v[212:215], v[8:11]
	v_mfma_f32_16x16x32_bf16 v[4:7], v[172:175], v[212:215], v[4:7]
	s_nop 0
	s_barrier
	s_mov_b64 s[36:37], 0
	s_mov_b64 s[30:31], -1
	s_mov_b64 s[34:35], 0x100
	s_cbranch_vccz .LBB0_2674
	s_and_b64 vcc, exec, s[12:13]
	s_cbranch_vccz .LBB0_2677
	s_barrier

.LBB0_2701:
	s_add_i32 s18, s91, 8
	s_cmp_ge_i32 s18, s67
	s_waitcnt vmcnt(0) lgkmcnt(0)
	s_barrier
	s_cbranch_scc1 .LBB0_2712
	s_waitcnt vmcnt(0)
	s_barrier
	s_setprio 0
	s_mov_b64 s[2:3], exec
	v_readlane_b32 s4, v243, 59
	v_readlane_b32 s5, v243, 60
	s_and_b64 s[4:5], s[2:3], s[4:5]
	s_mov_b32 s87, 0xf800000
	s_mov_b32 s90, 0x40e00000
	s_mov_b64 exec, s[4:5]
	s_cbranch_execz .LBB0_2750
	v_readlane_b32 s4, v243, 56
	s_waitcnt vmcnt(0) expcnt(0) lgkmcnt(0)
	s_nop 0
	v_mov_b32_e32 v1, s4
	ds_read_b32 v4, v1
	ds_read_b32 v2, v1 offset:4
	s_waitcnt lgkmcnt(1)
	v_cmp_ne_u32_e32 vcc, 0, v4
	s_cbranch_vccnz .LBB0_2718
	s_load_dwordx2 s[4:5], s[0:1], 0x0
	s_load_dword s6, s[0:1], 0x8
	s_mov_b32 s10, 0
	s_waitcnt lgkmcnt(0)
	s_mul_i32 s9, s5, s4
	s_mul_i32 s9, s9, s6
	s_branch .LBB0_2706

.LBB0_2919:
	s_waitcnt vmcnt(0)
	s_barrier
	s_setprio 0
	s_mov_b64 s[2:3], exec
	v_readlane_b32 s4, v243, 59
	v_readlane_b32 s5, v243, 60
	s_and_b64 s[4:5], s[2:3], s[4:5]
	s_mov_b64 exec, s[4:5]
	s_cbranch_execnz .LBB0_2920
	s_getpc_b64 s[98:99]
